# int8 quantise items: data loads issued before waiting for the column-scale load (vmcnt(16)), reciprocal math under the loads; flat_load re-encoded as global_load
# speedup vs baseline: 1.0043x; 1.0043x over previous
; __device__ __forceinline__ void cvt_item_i8(const float* src, int ld, int k0, int c0, unsigned char* dst, int Kd, int drow0, const float* cmx  , unsigned char* scr, int lane) {
;     const int c = lane & 7, q = lane >> 3;
;     const f32x4 cm = *(const f32x4*)(cmx + 4 * c);
;     f32x4 inv; inv[0] = cm[0] > 0.f ? 127.f / cm[0] : 0.f; inv[1] = cm[1] > 0.f ? 127.f / cm[1] : 0.f; inv[2] = cm[2] > 0.f ? 127.f / cm[2] : 0.f; inv[3] = cm[3] > 0.f ? 127.f / cm[3] : 0.f;
;     f32x4 v[4][4];
; #pragma unroll
;     for (int g = 0; g < 4; ++g)
; #pragma unroll
;         for (int j = 0; j < 4; ++j) v[g][j] = __builtin_nontemporal_load((const f32x4*)(src + (size_t)(k0 + 32 * g + 4 * q + j) * ld + c0 + 4 * c));
; template <int GRP>
; __device__ __forceinline__ void conv_item(Frame& F, int r) {
;     ...
;     else { constexpr int KBN = (GRP == 3) ? 16 : CMS_KB, I_E = KBN * 88; const int up = r / (8 * I_E); r %= (8 * I_E); const int e = r / I_E; r %= I_E; const int kb = r / 88, nb = r % 88, n0 = nb * 32, drow = (n0 >> 7) * 256 + up * 128 + (n0 & 127);
;         if (GRP == 3) cvt_item_i8(inptr(F, up ? IN_MU : IN_MG) + (size_t)e * D * DFE, DFE, kb * 128, n0, ws + WS_MGU + (size_t)e * 2 * DFE * D, D, drow, cmx + 2 * DFF + e * 2 * DFE + drow, scr, F.lane);
.LBB0_1405:
	s_add_i32 s0, s16, 0x1200
	s_mul_hi_i32 s1, s0, 0x2e8ba2e9
	s_lshr_b32 s6, s1, 31
	s_ashr_i32 s1, s1, 11
	s_add_i32 s1, s1, s6
	s_mul_i32 s6, s1, 0x2c00
	s_sub_i32 s0, s0, s6
	s_lshl_b32 s40, s1, 7
	s_mul_i32 s1, s0, 0xba3
	s_lshr_b32 s6, s1, 31
	s_ashr_i32 s1, s1, 22
	s_add_i32 s1, s1, s6
	s_mul_i32 s6, s1, 0x580
	s_sub_i32 s0, s0, s6
	s_sext_i32_i16 s6, s0
	s_mulk_i32 s6, 0xba3
	s_lshr_b32 s38, s6, 31
	s_ashr_i32 s6, s6, 18
	s_add_i32 s6, s6, s38
	s_sext_i32_i16 s38, s6
	s_mulk_i32 s6, 0x58
	s_sub_i32 s0, s0, s6
	s_sext_i32_i16 s6, s0
	s_lshl_b32 s0, s6, 5
	s_lshl_b32 s6, s6, 6
	s_and_b32 s6, s6, 0xffffff00
	s_and_b32 s41, s0, 0x60
	s_add_i32 s6, s6, s40
	s_add_i32 s39, s16, 0x3dff
	s_or_b32 s6, s6, s41
	s_cmpk_lt_u32 s39, 0x57ff
	s_cselect_b32 s39, s17, 0xa8
	v_or_b32_e32 v8, s6, v17
	s_add_i32 s39, s39, 0
	v_ashrrev_i32_e32 v9, 31, v8
	s_add_i32 s39, s39, 0x20200
	v_lshlrev_b64 v[98:99], 11, v[8:9]
	v_mov_b32_e32 v8, s39
	ds_read_b64 v[8:9], v8
	s_sext_i32_i16 s11, s1
	s_mul_i32 s9, s11, 0x1600000
	s_mul_hi_i32 s1, s11, 0x1600000
	s_mul_i32 s10, s11, 0xb00000
	s_waitcnt lgkmcnt(0)
	v_readfirstlane_b32 s39, v8
	v_readfirstlane_b32 s40, v9
	s_add_u32 s9, s39, s9
	s_addc_u32 s39, s40, s1
	s_lshl_b32 s38, s38, 7
	s_mul_hi_i32 s7, s11, 0xb00000
	s_add_u32 s10, s3, s10
	s_mul_hi_i32 s8, s11, 0x5800
	s_mulk_i32 s11, 0x5800
	s_addc_u32 s40, s4, s7
	s_add_u32 s1, s14, s11
	s_addc_u32 s8, s15, s8
	s_ashr_i32 s7, s6, 31
	v_or_b32_e32 v6, s6, v1
	v_or_b32_e32 v10, s6, v18
	v_or_b32_e32 v12, s6, v19
	s_lshl_b64 s[6:7], s[6:7], 2
	s_add_u32 s6, s1, s6
	s_addc_u32 s7, s8, s7
	s_ashr_i32 s1, s0, 31
	s_lshl_b64 s[0:1], s[0:1], 2
	v_or_b32_e32 v8, s38, v16
	s_add_u32 s0, s9, s0
	v_ashrrev_i32_e32 v11, 31, v10
	v_mul_i32_i24_e32 v8, 0x2c00, v8
	s_addc_u32 s1, s39, s1
	v_lshlrev_b64 v[100:101], 11, v[10:11]
	v_ashrrev_i32_e32 v9, 31, v8
	v_lshl_add_u64 v[10:11], s[0:1], 0, v[4:5]
	v_ashrrev_i32_e32 v7, 31, v6
	v_ashrrev_i32_e32 v13, 31, v12
	v_lshl_add_u64 v[10:11], v[10:11], 0, v[8:9]
	v_lshlrev_b64 v[14:15], 11, v[6:7]
	v_lshlrev_b64 v[6:7], 11, v[12:13]
	v_add_co_u32_e32 v12, vcc, s19, v10
	global_load_dwordx4 v[30:33], v4, s[6:7]
	s_nop 0
	v_addc_co_u32_e32 v13, vcc, 0, v11, vcc
	v_add_co_u32_e32 v42, vcc, s20, v10
	s_ashr_i32 s6, s38, 31
	s_nop 0
	v_addc_co_u32_e32 v43, vcc, 0, v11, vcc
	v_add_co_u32_e32 v46, vcc, s21, v10
	s_add_u32 s0, s10, s38
	s_nop 0
	v_addc_co_u32_e32 v47, vcc, 0, v11, vcc
	v_add_co_u32_e32 v50, vcc, s22, v10
	s_addc_u32 s1, s40, s6
	s_nop 0
	v_addc_co_u32_e32 v51, vcc, 0, v11, vcc
	v_add_co_u32_e32 v54, vcc, s23, v10
	v_lshl_add_u64 v[8:9], s[0:1], 0, v[2:3]
	s_nop 0
	v_addc_co_u32_e32 v55, vcc, 0, v11, vcc
	v_add_co_u32_e32 v58, vcc, s24, v10
	v_lshl_add_u64 v[6:7], v[8:9], 0, v[6:7]
	s_nop 0
	v_addc_co_u32_e32 v59, vcc, 0, v11, vcc
	v_add_co_u32_e32 v62, vcc, s25, v10
	s_addk_i32 s16, 0x200
	s_nop 0
	v_addc_co_u32_e32 v63, vcc, 0, v11, vcc
	v_add_co_u32_e32 v66, vcc, s26, v10
	s_cmpk_gt_i32 s16, 0x5ff
	s_nop 0
	v_addc_co_u32_e32 v67, vcc, 0, v11, vcc
	v_add_co_u32_e32 v70, vcc, s27, v10
	s_nop 0
	s_nop 0
	v_addc_co_u32_e32 v71, vcc, 0, v11, vcc
	v_add_co_u32_e32 v74, vcc, s28, v10
	s_nop 0
	s_nop 0
	v_addc_co_u32_e32 v75, vcc, 0, v11, vcc
	v_add_co_u32_e32 v78, vcc, s29, v10
	s_nop 0
	s_nop 0
	v_addc_co_u32_e32 v79, vcc, 0, v11, vcc
	v_add_co_u32_e32 v82, vcc, s30, v10
	s_nop 0
	s_nop 0
	v_addc_co_u32_e32 v83, vcc, 0, v11, vcc
	v_add_co_u32_e32 v86, vcc, s31, v10
	s_nop 0
	s_nop 0
	v_addc_co_u32_e32 v87, vcc, 0, v11, vcc
	v_add_co_u32_e32 v90, vcc, s34, v10
	s_nop 0
	s_nop 0
	v_addc_co_u32_e32 v91, vcc, 0, v11, vcc
	v_add_co_u32_e32 v94, vcc, s35, v10
	s_nop 0
	s_nop 0
	v_addc_co_u32_e32 v95, vcc, 0, v11, vcc
	global_load_dwordx4 v[34:37], v[10:11], off nt
	global_load_dwordx4 v[38:41], v[12:13], off offset:3072 nt
	s_nop 0
	global_load_dwordx4 v[42:45], v[42:43], off offset:2048 nt
	s_nop 0
	global_load_dwordx4 v[46:49], v[46:47], off offset:1024 nt
	s_nop 0
	global_load_dwordx4 v[50:53], v[50:51], off nt
	s_nop 0
	global_load_dwordx4 v[54:57], v[54:55], off offset:3072 nt
	s_nop 0
	global_load_dwordx4 v[58:61], v[58:59], off offset:2048 nt
	s_nop 0
	global_load_dwordx4 v[62:65], v[62:63], off offset:1024 nt
	s_nop 0
	global_load_dwordx4 v[66:69], v[66:67], off nt
	s_nop 0
	global_load_dwordx4 v[70:73], v[70:71], off offset:3072 nt
	s_nop 0
	global_load_dwordx4 v[74:77], v[74:75], off offset:2048 nt
	s_nop 0
	global_load_dwordx4 v[78:81], v[78:79], off offset:1024 nt
	s_nop 0
	global_load_dwordx4 v[82:85], v[82:83], off nt
	s_nop 0
	global_load_dwordx4 v[86:89], v[86:87], off offset:3072 nt
	s_nop 0
	global_load_dwordx4 v[90:93], v[90:91], off offset:2048 nt
	s_nop 0
	global_load_dwordx4 v[94:97], v[94:95], off offset:1024 nt
	s_waitcnt vmcnt(16)
; __device__ __forceinline__ unsigned pack_i8x4(float a, float b, float c, float d) {
;     const int ia = (int)rintf(fminf(fmaxf(a, -127.f), 127.f)), ib = (int)rintf(fminf(fmaxf(b, -127.f), 127.f)), ic = (int)rintf(fminf(fmaxf(c, -127.f), 127.f)), id = (int)rintf(fminf(fmaxf(d, -127.f), 127.f));
;     return (unsigned)(ia & 0xff) | ((unsigned)(ib & 0xff) << 8) | ((unsigned)(ic & 0xff) << 16) | ((unsigned)(id & 0xff) << 24);
; __device__ __forceinline__ void cvt_item_i8(const float* src, int ld, int k0, int c0, unsigned char* dst, int Kd, int drow0, const float* cmx  , unsigned char* scr, int lane) {
;     ...
;     f32x4 inv; inv[0] = cm[0] > 0.f ? 127.f / cm[0] : 0.f; inv[1] = cm[1] > 0.f ? 127.f / cm[1] : 0.f; inv[2] = cm[2] > 0.f ? 127.f / cm[2] : 0.f; inv[3] = cm[3] > 0.f ? 127.f / cm[3] : 0.f;
;     f32x4 v[4][4];
; #pragma unroll
;     for (int g = 0; g < 4; ++g)
; #pragma unroll
;         for (int j = 0; j < 4; ++j) v[g][j] = __builtin_nontemporal_load((const f32x4*)(src + (size_t)(k0 + 32 * g + 4 * q + j) * ld + c0 + 4 * c));
; #pragma unroll
;     for (int g = 0; g < 4; ++g)
; #pragma unroll
;         for (int i = 0; i < 4; ++i) *(unsigned*)(scr + (4 * c + i) * 132 + 32 * g + 4 * q) = pack_i8x4(v[g][0][i] * inv[i], v[g][1][i] * inv[i], v[g][2][i] * inv[i], v[g][3][i] * inv[i]);
	v_div_scale_f32 v29, s[0:1], v30, v30, s18
	v_rcp_f32_e32 v105, v29
	v_div_scale_f32 v103, s[0:1], v33, v33, s18
	v_fma_f32 v109, -v29, v105, 1.0
	v_rcp_f32_e32 v108, v103
	v_fmac_f32_e32 v105, v109, v105
	v_div_scale_f32 v102, s[8:9], s18, v32, s18
	v_lshl_add_u64 v[12:13], v[8:9], 0, v[98:99]
	v_div_scale_f32 v99, s[0:1], v31, v31, s18
	v_rcp_f32_e32 v106, v99
	v_lshl_add_u64 v[10:11], v[8:9], 0, v[14:15]
	v_lshl_add_u64 v[14:15], v[8:9], 0, v[100:101]
	v_div_scale_f32 v101, s[0:1], v32, v32, s18
	v_rcp_f32_e32 v107, v101
	v_div_scale_f32 v98, vcc, s18, v30, s18
	v_fma_f32 v110, -v99, v106, 1.0
	v_div_scale_f32 v100, s[6:7], s18, v31, s18
	v_fmac_f32_e32 v106, v110, v106
	v_mul_f32_e32 v109, v98, v105
	v_fma_f32 v111, -v101, v107, 1.0
	v_mul_f32_e32 v110, v100, v106
	v_fma_f32 v113, -v29, v109, v98
	v_fmac_f32_e32 v107, v111, v107
	v_fma_f32 v114, -v99, v110, v100
	v_fmac_f32_e32 v109, v113, v105
	v_fma_f32 v112, -v103, v108, 1.0
	v_mul_f32_e32 v111, v102, v107
	v_fmac_f32_e32 v110, v114, v106
	v_fma_f32 v29, -v29, v109, v98
	v_div_scale_f32 v104, s[10:11], s18, v33, s18
	v_fmac_f32_e32 v108, v112, v108
	v_fma_f32 v115, -v101, v111, v102
	v_fma_f32 v98, -v99, v110, v100
	v_div_fmas_f32 v29, v29, v105, v109
	s_mov_b64 vcc, s[6:7]
	v_mul_f32_e32 v112, v104, v108
	v_fmac_f32_e32 v111, v115, v107
	v_div_fixup_f32 v29, v29, v30, s18
	v_div_fmas_f32 v98, v98, v106, v110
	v_cmp_lt_f32_e32 vcc, 0, v30
	v_fma_f32 v116, -v103, v112, v104
	v_fma_f32 v99, -v101, v111, v102
	v_cndmask_b32_e32 v29, 0, v29, vcc
	s_mov_b64 vcc, s[8:9]
	v_fmac_f32_e32 v112, v116, v108
	v_div_fixup_f32 v30, v98, v31, s18
	v_div_fmas_f32 v98, v99, v107, v111
	v_cmp_lt_f32_e32 vcc, 0, v31
	v_fma_f32 v100, -v103, v112, v104
	v_div_fixup_f32 v31, v98, v32, s18
	v_cndmask_b32_e32 v30, 0, v30, vcc
	s_mov_b64 vcc, s[10:11]
	v_div_fmas_f32 v98, v100, v108, v112
	v_cmp_lt_f32_e32 vcc, 0, v32
	v_div_fixup_f32 v32, v98, v33, s18
	s_waitcnt vmcnt(0) lgkmcnt(0)
	v_mul_f32_e32 v34, v34, v29
	v_mul_f32_e32 v38, v29, v38
	v_mul_f32_e32 v42, v29, v42
	v_mul_f32_e32 v46, v29, v46
	v_mul_f32_e32 v50, v29, v50
	v_mul_f32_e32 v54, v29, v54
	v_mul_f32_e32 v58, v29, v58
	v_mul_f32_e32 v62, v29, v62
	v_mul_f32_e32 v66, v29, v66
	v_mul_f32_e32 v70, v29, v70
	v_mul_f32_e32 v74, v29, v74
	v_mul_f32_e32 v78, v29, v78
	v_mul_f32_e32 v82, v29, v82
	v_mul_f32_e32 v86, v29, v86
	v_cndmask_b32_e32 v31, 0, v31, vcc
	v_med3_f32 v34, v34, s36, v20
	v_med3_f32 v38, v38, s36, v20
	v_med3_f32 v42, v42, s36, v20
	v_med3_f32 v46, v46, s36, v20
	v_mul_f32_e32 v39, v30, v39
	v_mul_f32_e32 v43, v30, v43
	v_mul_f32_e32 v47, v30, v47
	v_med3_f32 v50, v50, s36, v20
	v_med3_f32 v54, v54, s36, v20
	v_mul_f32_e32 v55, v30, v55
	v_cmp_lt_f32_e32 vcc, 0, v33
	v_mul_f32_e32 v90, v29, v90
	v_mul_f32_e32 v35, v35, v30
	v_med3_f32 v58, v58, s36, v20
	v_med3_f32 v62, v62, s36, v20
	v_mul_f32_e32 v51, v30, v51
	v_mul_f32_e32 v59, v30, v59
	v_mul_f32_e32 v63, v30, v63
	v_med3_f32 v66, v66, s36, v20
	v_med3_f32 v70, v70, s36, v20
	v_med3_f32 v74, v74, s36, v20
	v_med3_f32 v78, v78, s36, v20
	v_mul_f32_e32 v71, v30, v71
	v_mul_f32_e32 v79, v30, v79
	v_med3_f32 v82, v82, s36, v20
	v_med3_f32 v86, v86, s36, v20
	v_mul_f32_e32 v87, v30, v87
	v_cndmask_b32_e32 v32, 0, v32, vcc
	v_rndne_f32_e32 v33, v34
	v_rndne_f32_e32 v34, v38
	v_rndne_f32_e32 v38, v42
	v_rndne_f32_e32 v42, v46
	v_med3_f32 v39, v39, s36, v20
	v_med3_f32 v43, v43, s36, v20
	v_med3_f32 v46, v47, s36, v20
	v_mul_f32_e32 v40, v31, v40
	v_mul_f32_e32 v47, v31, v48
	v_rndne_f32_e32 v48, v50
	v_rndne_f32_e32 v50, v54
	v_med3_f32 v55, v55, s36, v20
	v_mul_f32_e32 v56, v31, v56
	v_mul_f32_e32 v29, v29, v94
	v_mul_f32_e32 v67, v30, v67
	v_mul_f32_e32 v75, v30, v75
	v_med3_f32 v90, v90, s36, v20
	v_mul_f32_e32 v83, v30, v83
	v_mul_f32_e32 v91, v30, v91
	v_med3_f32 v35, v35, s36, v20
	v_mul_f32_e32 v36, v36, v31
	v_mul_f32_e32 v44, v31, v44
	v_rndne_f32_e32 v54, v58
	v_rndne_f32_e32 v58, v62
	v_med3_f32 v51, v51, s36, v20
	v_med3_f32 v59, v59, s36, v20
	v_med3_f32 v62, v63, s36, v20
	v_mul_f32_e32 v52, v31, v52
	v_mul_f32_e32 v60, v31, v60
	v_mul_f32_e32 v63, v31, v64
	v_rndne_f32_e32 v64, v66
	v_rndne_f32_e32 v66, v70
	v_rndne_f32_e32 v70, v74
	v_rndne_f32_e32 v74, v78
	v_med3_f32 v71, v71, s36, v20
	v_med3_f32 v78, v79, s36, v20
	v_mul_f32_e32 v72, v31, v72
	v_mul_f32_e32 v79, v31, v80
	v_rndne_f32_e32 v80, v82
	v_rndne_f32_e32 v82, v86
	v_med3_f32 v87, v87, s36, v20
	v_mul_f32_e32 v88, v31, v88
	v_cvt_i32_f32_e32 v34, v34
	v_rndne_f32_e32 v39, v39
	v_rndne_f32_e32 v43, v43
	v_med3_f32 v40, v40, s36, v20
	v_mul_f32_e32 v41, v32, v41
	v_cvt_i32_f32_e32 v50, v50
	v_rndne_f32_e32 v55, v55
	v_med3_f32 v56, v56, s36, v20
	v_mul_f32_e32 v57, v32, v57
	v_med3_f32 v29, v29, s36, v20
	v_mul_f32_e32 v30, v30, v95
	v_med3_f32 v67, v67, s36, v20
	v_med3_f32 v75, v75, s36, v20
	v_mul_f32_e32 v68, v31, v68
	v_mul_f32_e32 v76, v31, v76
	v_rndne_f32_e32 v86, v90
	v_med3_f32 v83, v83, s36, v20
	v_med3_f32 v90, v91, s36, v20
	v_mul_f32_e32 v84, v31, v84
	v_mul_f32_e32 v91, v31, v92
	v_cvt_i32_f32_e32 v33, v33
	v_cvt_i32_f32_sdwa v38, v38 dst_sel:WORD_1 dst_unused:UNUSED_PAD src0_sel:DWORD
	v_rndne_f32_e32 v35, v35
	v_med3_f32 v36, v36, s36, v20
	v_med3_f32 v44, v44, s36, v20
	v_mul_f32_e32 v37, v37, v32
	v_mul_f32_e32 v45, v32, v45
	v_cvt_i32_f32_e32 v48, v48
	v_cvt_i32_f32_sdwa v54, v54 dst_sel:WORD_1 dst_unused:UNUSED_PAD src0_sel:DWORD
	v_rndne_f32_e32 v51, v51
	v_rndne_f32_e32 v59, v59
	v_med3_f32 v52, v52, s36, v20
	v_med3_f32 v60, v60, s36, v20
	v_mul_f32_e32 v53, v32, v53
	v_mul_f32_e32 v61, v32, v61
	v_cvt_i32_f32_e32 v66, v66
	v_rndne_f32_e32 v71, v71
	v_med3_f32 v72, v72, s36, v20
; __device__ __forceinline__ unsigned pack_i8x4(float a, float b, float c, float d) {
;     const int ia = (int)rintf(fminf(fmaxf(a, -127.f), 127.f)), ib = (int)rintf(fminf(fmaxf(b, -127.f), 127.f)), ic = (int)rintf(fminf(fmaxf(c, -127.f), 127.f)), id = (int)rintf(fminf(fmaxf(d, -127.f), 127.f));
;     return (unsigned)(ia & 0xff) | ((unsigned)(ib & 0xff) << 8) | ((unsigned)(ic & 0xff) << 16) | ((unsigned)(id & 0xff) << 24);
; __device__ __forceinline__ void cvt_item_i8(const float* src, int ld, int k0, int c0, unsigned char* dst, int Kd, int drow0, const float* cmx  , unsigned char* scr, int lane) {
;     ...
; #pragma unroll
;     for (int g = 0; g < 4; ++g)
; #pragma unroll
;         for (int i = 0; i < 4; ++i) *(unsigned*)(scr + (4 * c + i) * 132 + 32 * g + 4 * q) = pack_i8x4(v[g][0][i] * inv[i], v[g][1][i] * inv[i], v[g][2][i] * inv[i], v[g][3][i] * inv[i]);
	v_mul_f32_e32 v73, v32, v73
	v_cvt_i32_f32_e32 v82, v82
	v_rndne_f32_e32 v87, v87
	v_med3_f32 v88, v88, s36, v20
	v_mul_f32_e32 v89, v32, v89
	v_cvt_i32_f32_e32 v39, v39
	v_cvt_i32_f32_sdwa v43, v43 dst_sel:WORD_1 dst_unused:UNUSED_PAD src0_sel:DWORD
	v_rndne_f32_e32 v40, v40
	v_med3_f32 v41, v41, s36, v20
	v_cvt_i32_f32_e32 v55, v55
	v_rndne_f32_e32 v56, v56
	v_med3_f32 v57, v57, s36, v20
	v_rndne_f32_e32 v29, v29
	v_med3_f32 v30, v30, s36, v20
	v_mul_f32_e32 v31, v31, v96
	v_cvt_i32_f32_sdwa v42, v42 dst_sel:BYTE_3 dst_unused:UNUSED_PAD src0_sel:DWORD
	v_rndne_f32_e32 v46, v46
	v_med3_f32 v47, v47, s36, v20
	v_mul_f32_e32 v49, v32, v49
	v_cvt_i32_f32_sdwa v58, v58 dst_sel:BYTE_3 dst_unused:UNUSED_PAD src0_sel:DWORD
	v_rndne_f32_e32 v62, v62
	v_med3_f32 v63, v63, s36, v20
	v_mul_f32_e32 v65, v32, v65
	v_cvt_i32_f32_e32 v64, v64
	v_cvt_i32_f32_sdwa v70, v70 dst_sel:WORD_1 dst_unused:UNUSED_PAD src0_sel:DWORD
	v_rndne_f32_e32 v67, v67
	v_rndne_f32_e32 v75, v75
	v_med3_f32 v68, v68, s36, v20
	v_med3_f32 v76, v76, s36, v20
	v_mul_f32_e32 v69, v32, v69
	v_mul_f32_e32 v77, v32, v77
	v_cvt_i32_f32_e32 v80, v80
	v_cvt_i32_f32_sdwa v86, v86 dst_sel:WORD_1 dst_unused:UNUSED_PAD src0_sel:DWORD
	v_rndne_f32_e32 v83, v83
	v_rndne_f32_e32 v90, v90
	v_med3_f32 v84, v84, s36, v20
	v_med3_f32 v91, v91, s36, v20
	v_mul_f32_e32 v85, v32, v85
	v_mul_f32_e32 v92, v32, v93
	v_cvt_i32_f32_e32 v35, v35
	v_rndne_f32_e32 v36, v36
	v_rndne_f32_e32 v44, v44
	v_med3_f32 v37, v37, s36, v20
	v_med3_f32 v45, v45, s36, v20
	v_cvt_i32_f32_e32 v51, v51
	v_cvt_i32_f32_sdwa v59, v59 dst_sel:WORD_1 dst_unused:UNUSED_PAD src0_sel:DWORD
	v_rndne_f32_e32 v52, v52
	v_rndne_f32_e32 v60, v60
	v_med3_f32 v53, v53, s36, v20
	v_med3_f32 v61, v61, s36, v20
	v_cvt_i32_f32_e32 v71, v71
	v_rndne_f32_e32 v72, v72
	v_med3_f32 v73, v73, s36, v20
	v_cvt_i32_f32_e32 v87, v87
	v_rndne_f32_e32 v88, v88
	v_med3_f32 v89, v89, s36, v20
	v_cvt_i32_f32_e32 v40, v40
	v_rndne_f32_e32 v41, v41
	v_cvt_i32_f32_e32 v56, v56
	v_rndne_f32_e32 v57, v57
	v_cvt_i32_f32_sdwa v74, v74 dst_sel:BYTE_3 dst_unused:UNUSED_PAD src0_sel:DWORD
	v_rndne_f32_e32 v78, v78
	v_med3_f32 v79, v79, s36, v20
	v_mul_f32_e32 v81, v32, v81
	v_cvt_i32_f32_sdwa v29, v29 dst_sel:BYTE_3 dst_unused:UNUSED_PAD src0_sel:DWORD
	v_rndne_f32_e32 v30, v30
	v_med3_f32 v31, v31, s36, v20
	v_mul_f32_e32 v32, v32, v97
	v_cvt_i32_f32_sdwa v46, v46 dst_sel:BYTE_3 dst_unused:UNUSED_PAD src0_sel:DWORD
	v_rndne_f32_e32 v47, v47
	v_med3_f32 v49, v49, s36, v20
	v_cvt_i32_f32_sdwa v62, v62 dst_sel:BYTE_3 dst_unused:UNUSED_PAD src0_sel:DWORD
	v_rndne_f32_e32 v63, v63
	v_med3_f32 v65, v65, s36, v20
	v_cvt_i32_f32_e32 v67, v67
	v_cvt_i32_f32_sdwa v75, v75 dst_sel:WORD_1 dst_unused:UNUSED_PAD src0_sel:DWORD
	v_rndne_f32_e32 v68, v68
	v_rndne_f32_e32 v76, v76
	v_med3_f32 v69, v69, s36, v20
	v_med3_f32 v77, v77, s36, v20
	v_cvt_i32_f32_e32 v83, v83
	v_cvt_i32_f32_sdwa v90, v90 dst_sel:WORD_1 dst_unused:UNUSED_PAD src0_sel:DWORD
	v_rndne_f32_e32 v84, v84
	v_rndne_f32_e32 v91, v91
	v_med3_f32 v85, v85, s36, v20
	v_med3_f32 v92, v92, s36, v20
	v_cvt_i32_f32_e32 v36, v36
	v_cvt_i32_f32_sdwa v44, v44 dst_sel:WORD_1 dst_unused:UNUSED_PAD src0_sel:DWORD
	v_rndne_f32_e32 v37, v37
	v_rndne_f32_e32 v45, v45
	v_cvt_i32_f32_e32 v52, v52
	v_cvt_i32_f32_sdwa v60, v60 dst_sel:WORD_1 dst_unused:UNUSED_PAD src0_sel:DWORD
	v_rndne_f32_e32 v53, v53
	v_rndne_f32_e32 v61, v61
	v_cvt_i32_f32_e32 v72, v72
	v_rndne_f32_e32 v73, v73
	v_cvt_i32_f32_e32 v88, v88
	v_rndne_f32_e32 v89, v89
	v_cvt_i32_f32_e32 v41, v41
	v_cvt_i32_f32_e32 v57, v57
	v_cvt_i32_f32_sdwa v78, v78 dst_sel:BYTE_3 dst_unused:UNUSED_PAD src0_sel:DWORD
	v_rndne_f32_e32 v79, v79
	v_med3_f32 v81, v81, s36, v20
	v_cvt_i32_f32_sdwa v30, v30 dst_sel:BYTE_3 dst_unused:UNUSED_PAD src0_sel:DWORD
	v_rndne_f32_e32 v31, v31
	v_med3_f32 v32, v32, s36, v20
	v_cvt_i32_f32_sdwa v47, v47 dst_sel:BYTE_3 dst_unused:UNUSED_PAD src0_sel:DWORD
	v_rndne_f32_e32 v49, v49
	v_cvt_i32_f32_sdwa v63, v63 dst_sel:BYTE_3 dst_unused:UNUSED_PAD src0_sel:DWORD
	v_rndne_f32_e32 v65, v65
	v_cvt_i32_f32_e32 v68, v68
	v_cvt_i32_f32_sdwa v76, v76 dst_sel:WORD_1 dst_unused:UNUSED_PAD src0_sel:DWORD
	v_rndne_f32_e32 v69, v69
	v_rndne_f32_e32 v77, v77
	v_cvt_i32_f32_e32 v84, v84
; __device__ __forceinline__ void cvt_item_i8(const float* src, int ld, int k0, int c0, unsigned char* dst, int Kd, int drow0, const float* cmx  , unsigned char* scr, int lane) {
;     ...
; #pragma unroll
;     for (int g = 0; g < 4; ++g)
; #pragma unroll
;         for (int i = 0; i < 4; ++i) *(unsigned*)(scr + (4 * c + i) * 132 + 32 * g + 4 * q) = pack_i8x4(v[g][0][i] * inv[i], v[g][1][i] * inv[i], v[g][2][i] * inv[i], v[g][3][i] * inv[i]);
;     asm volatile("s_waitcnt lgkmcnt(0)" ::: "memory");
; #pragma unroll
;     for (int r = 0; r < 4; ++r) { const int n = 8 * r + (lane >> 3), ch = lane & 7; const unsigned char* p = scr + n * 132 + ch * 16;
;         u32x4 o; o.x = *(const unsigned*)(p); o.y = *(const unsigned*)(p + 4); o.z = *(const unsigned*)(p + 8); o.w = *(const unsigned*)(p + 12);
;         *(u32x4*)(dst + (size_t)(drow0 + n) * Kd + k0 + 16 * ch) = o; }
;     asm volatile("s_waitcnt lgkmcnt(0)" ::: "memory");
	v_cvt_i32_f32_sdwa v91, v91 dst_sel:WORD_1 dst_unused:UNUSED_PAD src0_sel:DWORD
	v_rndne_f32_e32 v85, v85
	v_rndne_f32_e32 v92, v92
	v_cvt_i32_f32_e32 v37, v37
	v_cvt_i32_f32_sdwa v45, v45 dst_sel:WORD_1 dst_unused:UNUSED_PAD src0_sel:DWORD
	v_cvt_i32_f32_e32 v53, v53
	v_cvt_i32_f32_sdwa v61, v61 dst_sel:WORD_1 dst_unused:UNUSED_PAD src0_sel:DWORD
	v_cvt_i32_f32_e32 v73, v73
	v_cvt_i32_f32_e32 v89, v89
	v_lshlrev_b32_e32 v34, 8, v34
	v_lshlrev_b32_e32 v50, 8, v50
	v_cvt_i32_f32_sdwa v79, v79 dst_sel:BYTE_3 dst_unused:UNUSED_PAD src0_sel:DWORD
	v_rndne_f32_e32 v81, v81
	v_cvt_i32_f32_sdwa v31, v31 dst_sel:BYTE_3 dst_unused:UNUSED_PAD src0_sel:DWORD
	v_rndne_f32_e32 v32, v32
	v_cvt_i32_f32_sdwa v49, v49 dst_sel:BYTE_3 dst_unused:UNUSED_PAD src0_sel:DWORD
	v_cvt_i32_f32_sdwa v65, v65 dst_sel:BYTE_3 dst_unused:UNUSED_PAD src0_sel:DWORD
	v_cvt_i32_f32_e32 v69, v69
	v_cvt_i32_f32_sdwa v77, v77 dst_sel:WORD_1 dst_unused:UNUSED_PAD src0_sel:DWORD
	v_cvt_i32_f32_e32 v85, v85
	v_cvt_i32_f32_sdwa v92, v92 dst_sel:WORD_1 dst_unused:UNUSED_PAD src0_sel:DWORD
	v_and_b32_e32 v38, 0xff0000, v38
	v_and_b32_e32 v54, 0xff0000, v54
	v_lshlrev_b32_e32 v66, 8, v66
	v_lshlrev_b32_e32 v82, 8, v82
	v_perm_b32 v33, v34, v33, s37
	v_lshlrev_b32_e32 v34, 8, v39
	v_and_b32_e32 v39, 0xff0000, v43
	v_perm_b32 v43, v50, v48, s37
	v_lshlrev_b32_e32 v48, 8, v55
	v_cvt_i32_f32_sdwa v81, v81 dst_sel:BYTE_3 dst_unused:UNUSED_PAD src0_sel:DWORD
	v_cvt_i32_f32_sdwa v32, v32 dst_sel:BYTE_3 dst_unused:UNUSED_PAD src0_sel:DWORD
	v_and_b32_e32 v70, 0xff0000, v70
	v_and_b32_e32 v86, 0xff0000, v86
	v_and_b32_e32 v50, 0xff0000, v59
	v_perm_b32 v55, v66, v64, s37
	v_lshlrev_b32_e32 v59, 8, v71
	v_perm_b32 v66, v82, v80, s37
	v_lshlrev_b32_e32 v71, 8, v87
	v_or3_b32 v33, v33, v38, v42
	v_perm_b32 v34, v34, v35, s37
	v_lshlrev_b32_e32 v35, 8, v40
	v_or3_b32 v40, v43, v54, v58
	v_perm_b32 v42, v48, v51, s37
	v_lshlrev_b32_e32 v43, 8, v56
	v_and_b32_e32 v64, 0xff0000, v75
	v_and_b32_e32 v75, 0xff0000, v90
	v_and_b32_e32 v38, 0xff0000, v44
	v_and_b32_e32 v44, 0xff0000, v60
	v_or3_b32 v48, v55, v70, v74
	v_perm_b32 v51, v59, v67, s37
	v_lshlrev_b32_e32 v54, 8, v72
	v_or3_b32 v29, v66, v86, v29
	v_perm_b32 v56, v71, v83, s37
	v_lshlrev_b32_e32 v58, 8, v88
	v_or3_b32 v34, v34, v39, v46
	v_perm_b32 v35, v35, v36, s37
	v_lshlrev_b32_e32 v36, 8, v41
	ds_write2_b32 v21, v33, v40 offset1:8
	v_or3_b32 v33, v42, v50, v62
	v_perm_b32 v40, v43, v52, s37
	v_lshlrev_b32_e32 v41, 8, v57
	v_and_b32_e32 v55, 0xff0000, v76
	v_and_b32_e32 v59, 0xff0000, v91
	v_and_b32_e32 v39, 0xff0000, v45
	v_and_b32_e32 v42, 0xff0000, v61
	v_or3_b32 v43, v51, v64, v78
	v_perm_b32 v45, v54, v68, s37
	v_lshlrev_b32_e32 v46, 8, v73
	ds_write2_b32 v21, v48, v29 offset0:16 offset1:24
	v_or3_b32 v29, v56, v75, v30
	v_perm_b32 v30, v58, v84, s37
	v_lshlrev_b32_e32 v48, 8, v89
	v_or3_b32 v35, v35, v38, v47
	v_perm_b32 v36, v36, v37, s37
	ds_write2_b32 v21, v34, v33 offset0:33 offset1:41
	v_or3_b32 v33, v40, v44, v63
	v_perm_b32 v34, v41, v53, s37
	v_and_b32_e32 v50, 0xff0000, v77
	v_and_b32_e32 v51, 0xff0000, v92
	v_or3_b32 v37, v45, v55, v79
	v_perm_b32 v38, v46, v69, s37
	ds_write2_b32 v21, v43, v29 offset0:49 offset1:57
	v_or3_b32 v29, v30, v59, v31
	v_perm_b32 v30, v48, v85, s37
	v_or3_b32 v31, v36, v39, v49
	ds_write2_b32 v21, v35, v33 offset0:66 offset1:74
	v_or3_b32 v33, v34, v42, v65
	v_or3_b32 v34, v38, v50, v81
	ds_write2_b32 v21, v37, v29 offset0:82 offset1:90
	v_or3_b32 v29, v30, v51, v32
	ds_write2_b32 v21, v31, v33 offset0:99 offset1:107
	ds_write2_b32 v21, v34, v29 offset0:115 offset1:123
	s_waitcnt lgkmcnt(0)
	ds_read2_b32 v[30:31], v22 offset1:1
	ds_read2_b32 v[32:33], v22 offset0:2 offset1:3
	ds_read2_b32 v[34:35], v23 offset1:1
	ds_read2_b32 v[36:37], v24 offset1:1
	ds_read2_b32 v[38:39], v25 offset1:1
	ds_read2_b32 v[40:41], v26 offset1:1
	ds_read2_b32 v[42:43], v27 offset1:1
	ds_read2_b32 v[44:45], v28 offset1:1
	s_waitcnt lgkmcnt(6)
	global_store_dwordx4 v[10:11], v[30:33], off
	s_waitcnt lgkmcnt(4)
	global_store_dwordx4 v[12:13], v[34:37], off
	s_waitcnt lgkmcnt(2)
	global_store_dwordx4 v[14:15], v[38:41], off
	s_waitcnt lgkmcnt(0)
	global_store_dwordx4 v[6:7], v[42:45], off
	s_waitcnt lgkmcnt(0)
	s_cbranch_scc0 .LBB0_1405

; __device__ __forceinline__ void cvt_item_i8(const float* src, int ld, int k0, int c0, unsigned char* dst, int Kd, int drow0, const float* cmx  , unsigned char* scr, int lane) {
;     const int c = lane & 7, q = lane >> 3;
;     const f32x4 cm = *(const f32x4*)(cmx + 4 * c);
;     f32x4 inv; inv[0] = cm[0] > 0.f ? 127.f / cm[0] : 0.f; inv[1] = cm[1] > 0.f ? 127.f / cm[1] : 0.f; inv[2] = cm[2] > 0.f ? 127.f / cm[2] : 0.f; inv[3] = cm[3] > 0.f ? 127.f / cm[3] : 0.f;
;     f32x4 v[4][4];
; #pragma unroll
;     for (int g = 0; g < 4; ++g)
; #pragma unroll
;         for (int j = 0; j < 4; ++j) v[g][j] = __builtin_nontemporal_load((const f32x4*)(src + (size_t)(k0 + 32 * g + 4 * q + j) * ld + c0 + 4 * c));
; template <int GRP>
; __device__ __forceinline__ void conv_item(Frame& F, int r) {
;     ...
;     else { constexpr int KBN = (GRP == 3) ? 16 : CMS_KB, I_E = KBN * 88; const int up = r / (8 * I_E); r %= (8 * I_E); const int e = r / I_E; r %= I_E; const int kb = r / 88, nb = r % 88, n0 = nb * 32, drow = (n0 >> 7) * 256 + up * 128 + (n0 & 127);
;         if (GRP == 3) cvt_item_i8(inptr(F, up ? IN_MU : IN_MG) + (size_t)e * D * DFE, DFE, kb * 128, n0, ws + WS_MGU + (size_t)e * 2 * DFE * D, D, drow, cmx + 2 * DFF + e * 2 * DFE + drow, scr, F.lane);
;     ...
;     for (int it = first + F.gw; it < N; it += F.NGW) conv_item<GRP>(F, it);
.LBB0_1672:
	s_mul_hi_i32 s0, s3, 0x2e8ba2e9
	s_lshr_b32 s1, s0, 31
	s_ashr_i32 s0, s0, 11
	s_add_i32 s0, s0, s1
	s_mul_i32 s1, s0, 0xffffd400
	s_lshl_b32 s6, s0, 7
	s_add_i32 s0, s3, s1
	s_mul_i32 s1, s0, 0xba3
	s_lshr_b32 s7, s1, 31
	s_ashr_i32 s1, s1, 22
	s_add_i32 s1, s1, s7
	s_mul_i32 s7, s1, 0x580
	s_sub_i32 s0, s0, s7
	s_sext_i32_i16 s36, s0
	s_mulk_i32 s36, 0xba3
	s_lshr_b32 s38, s36, 31
	s_ashr_i32 s36, s36, 18
	s_add_i32 s38, s36, s38
	s_sext_i32_i16 s36, s38
	s_mulk_i32 s38, 0x58
	s_sub_i32 s0, s0, s38
	s_sext_i32_i16 s38, s0
	s_lshl_b32 s0, s38, 5
	s_lshl_b32 s38, s38, 6
	s_and_b32 s38, s38, 0xffffff00
	s_and_b32 s39, s0, 0x60
	s_add_i32 s38, s38, s6
	s_add_i32 s37, s3, 0x2bff
	s_or_b32 s6, s38, s39
	s_cmpk_lt_u32 s37, 0x57ff
	s_cselect_b32 s37, s15, 0xa8
	v_or_b32_e32 v8, s6, v17
	s_add_i32 s37, s37, 0
	v_ashrrev_i32_e32 v9, 31, v8
	s_add_i32 s37, s37, 0x20200
	v_lshlrev_b64 v[98:99], 11, v[8:9]
	v_mov_b32_e32 v8, s37
	ds_read_b64 v[8:9], v8
	s_sext_i32_i16 s11, s1
	s_mul_i32 s9, s11, 0x1600000
	s_mul_hi_i32 s1, s11, 0x1600000
	s_mul_i32 s10, s11, 0xb00000
	s_waitcnt lgkmcnt(0)
	v_readfirstlane_b32 s37, v8
	v_readfirstlane_b32 s38, v9
	s_add_u32 s9, s37, s9
	s_addc_u32 s37, s38, s1
	s_lshl_b32 s36, s36, 7
	s_mul_hi_i32 s7, s11, 0xb00000
	s_add_u32 s10, s4, s10
	s_mul_hi_i32 s8, s11, 0x5800
	s_mulk_i32 s11, 0x5800
	s_addc_u32 s38, s12, s7
	s_add_u32 s1, s13, s11
	s_addc_u32 s8, s14, s8
	s_ashr_i32 s7, s6, 31
	v_or_b32_e32 v6, s6, v1
	v_or_b32_e32 v10, s6, v18
	v_or_b32_e32 v12, s6, v19
	s_lshl_b64 s[6:7], s[6:7], 2
	s_add_u32 s6, s1, s6
	s_addc_u32 s7, s8, s7
	s_ashr_i32 s1, s0, 31
	s_lshl_b64 s[0:1], s[0:1], 2
	v_or_b32_e32 v8, s36, v16
	s_add_u32 s0, s9, s0
	v_ashrrev_i32_e32 v11, 31, v10
	v_mul_i32_i24_e32 v8, 0x2c00, v8
	s_addc_u32 s1, s37, s1
	v_lshlrev_b64 v[100:101], 11, v[10:11]
	v_ashrrev_i32_e32 v9, 31, v8
	v_lshl_add_u64 v[10:11], s[0:1], 0, v[4:5]
	v_ashrrev_i32_e32 v7, 31, v6
	v_ashrrev_i32_e32 v13, 31, v12
	v_lshl_add_u64 v[10:11], v[10:11], 0, v[8:9]
	v_lshlrev_b64 v[14:15], 11, v[6:7]
	v_lshlrev_b64 v[6:7], 11, v[12:13]
	v_add_co_u32_e32 v12, vcc, s17, v10
	global_load_dwordx4 v[30:33], v4, s[6:7]
	s_nop 0
	v_addc_co_u32_e32 v13, vcc, 0, v11, vcc
	v_add_co_u32_e32 v42, vcc, s18, v10
	s_ashr_i32 s6, s36, 31
	s_nop 0
	v_addc_co_u32_e32 v43, vcc, 0, v11, vcc
	v_add_co_u32_e32 v46, vcc, s19, v10
	s_add_u32 s0, s10, s36
	s_nop 0
	v_addc_co_u32_e32 v47, vcc, 0, v11, vcc
	v_add_co_u32_e32 v50, vcc, s20, v10
	s_addc_u32 s1, s38, s6
	s_nop 0
	v_addc_co_u32_e32 v51, vcc, 0, v11, vcc
	v_add_co_u32_e32 v54, vcc, s21, v10
	v_lshl_add_u64 v[8:9], s[0:1], 0, v[2:3]
	s_nop 0
	v_addc_co_u32_e32 v55, vcc, 0, v11, vcc
	v_add_co_u32_e32 v58, vcc, s22, v10
	v_lshl_add_u64 v[6:7], v[8:9], 0, v[6:7]
	s_nop 0
	v_addc_co_u32_e32 v59, vcc, 0, v11, vcc
	v_add_co_u32_e32 v62, vcc, s23, v10
	s_add_i32 s3, s3, s40
	s_nop 0
	v_addc_co_u32_e32 v63, vcc, 0, v11, vcc
	v_add_co_u32_e32 v66, vcc, s24, v10
	s_cmpk_lt_i32 s3, 0x5800
	s_nop 0
	v_addc_co_u32_e32 v67, vcc, 0, v11, vcc
	v_add_co_u32_e32 v70, vcc, s25, v10
	s_nop 0
	s_nop 0
	v_addc_co_u32_e32 v71, vcc, 0, v11, vcc
	v_add_co_u32_e32 v74, vcc, s26, v10
	s_nop 0
	s_nop 0
	v_addc_co_u32_e32 v75, vcc, 0, v11, vcc
	v_add_co_u32_e32 v78, vcc, s27, v10
	s_nop 0
	s_nop 0
	v_addc_co_u32_e32 v79, vcc, 0, v11, vcc
	v_add_co_u32_e32 v82, vcc, s28, v10
	s_nop 0
	s_nop 0
	v_addc_co_u32_e32 v83, vcc, 0, v11, vcc
	v_add_co_u32_e32 v86, vcc, s29, v10
	s_nop 0
	s_nop 0
	v_addc_co_u32_e32 v87, vcc, 0, v11, vcc
	v_add_co_u32_e32 v90, vcc, s30, v10
	s_nop 0
	s_nop 0
	v_addc_co_u32_e32 v91, vcc, 0, v11, vcc
	v_add_co_u32_e32 v94, vcc, s31, v10
	s_nop 0
	s_nop 0
	v_addc_co_u32_e32 v95, vcc, 0, v11, vcc
	global_load_dwordx4 v[34:37], v[10:11], off nt
	global_load_dwordx4 v[38:41], v[12:13], off offset:3072 nt
	s_nop 0
	global_load_dwordx4 v[42:45], v[42:43], off offset:2048 nt
	s_nop 0
	global_load_dwordx4 v[46:49], v[46:47], off offset:1024 nt
	s_nop 0
	global_load_dwordx4 v[50:53], v[50:51], off nt
	s_nop 0
	global_load_dwordx4 v[54:57], v[54:55], off offset:3072 nt
	s_nop 0
	global_load_dwordx4 v[58:61], v[58:59], off offset:2048 nt
	s_nop 0
	global_load_dwordx4 v[62:65], v[62:63], off offset:1024 nt
	s_nop 0
	global_load_dwordx4 v[66:69], v[66:67], off nt
	s_nop 0
	global_load_dwordx4 v[70:73], v[70:71], off offset:3072 nt
	s_nop 0
	global_load_dwordx4 v[74:77], v[74:75], off offset:2048 nt
	s_nop 0
	global_load_dwordx4 v[78:81], v[78:79], off offset:1024 nt
	s_nop 0
	global_load_dwordx4 v[82:85], v[82:83], off nt
	s_nop 0
	global_load_dwordx4 v[86:89], v[86:87], off offset:3072 nt
	s_nop 0
	global_load_dwordx4 v[90:93], v[90:91], off offset:2048 nt
	s_nop 0
	global_load_dwordx4 v[94:97], v[94:95], off offset:1024 nt
	s_waitcnt vmcnt(16)
; __device__ __forceinline__ unsigned pack_i8x4(float a, float b, float c, float d) {
;     const int ia = (int)rintf(fminf(fmaxf(a, -127.f), 127.f)), ib = (int)rintf(fminf(fmaxf(b, -127.f), 127.f)), ic = (int)rintf(fminf(fmaxf(c, -127.f), 127.f)), id = (int)rintf(fminf(fmaxf(d, -127.f), 127.f));
;     return (unsigned)(ia & 0xff) | ((unsigned)(ib & 0xff) << 8) | ((unsigned)(ic & 0xff) << 16) | ((unsigned)(id & 0xff) << 24);
; __device__ __forceinline__ void cvt_item_i8(const float* src, int ld, int k0, int c0, unsigned char* dst, int Kd, int drow0, const float* cmx  , unsigned char* scr, int lane) {
;     ...
;     f32x4 inv; inv[0] = cm[0] > 0.f ? 127.f / cm[0] : 0.f; inv[1] = cm[1] > 0.f ? 127.f / cm[1] : 0.f; inv[2] = cm[2] > 0.f ? 127.f / cm[2] : 0.f; inv[3] = cm[3] > 0.f ? 127.f / cm[3] : 0.f;
;     f32x4 v[4][4];
; #pragma unroll
;     for (int g = 0; g < 4; ++g)
; #pragma unroll
;         for (int j = 0; j < 4; ++j) v[g][j] = __builtin_nontemporal_load((const f32x4*)(src + (size_t)(k0 + 32 * g + 4 * q + j) * ld + c0 + 4 * c));
; #pragma unroll
;     for (int g = 0; g < 4; ++g)
; #pragma unroll
;         for (int i = 0; i < 4; ++i) *(unsigned*)(scr + (4 * c + i) * 132 + 32 * g + 4 * q) = pack_i8x4(v[g][0][i] * inv[i], v[g][1][i] * inv[i], v[g][2][i] * inv[i], v[g][3][i] * inv[i]);
	v_div_scale_f32 v29, s[0:1], v30, v30, s16
	v_rcp_f32_e32 v105, v29
	v_div_scale_f32 v103, s[0:1], v33, v33, s16
	v_fma_f32 v109, -v29, v105, 1.0
	v_rcp_f32_e32 v108, v103
	v_fmac_f32_e32 v105, v109, v105
	v_div_scale_f32 v102, s[8:9], s16, v32, s16
	v_lshl_add_u64 v[12:13], v[8:9], 0, v[98:99]
	v_div_scale_f32 v99, s[0:1], v31, v31, s16
	v_rcp_f32_e32 v106, v99
	v_lshl_add_u64 v[10:11], v[8:9], 0, v[14:15]
	v_lshl_add_u64 v[14:15], v[8:9], 0, v[100:101]
	v_div_scale_f32 v101, s[0:1], v32, v32, s16
	v_rcp_f32_e32 v107, v101
	v_div_scale_f32 v98, vcc, s16, v30, s16
	v_fma_f32 v110, -v99, v106, 1.0
	v_div_scale_f32 v100, s[6:7], s16, v31, s16
	v_fmac_f32_e32 v106, v110, v106
	v_mul_f32_e32 v109, v98, v105
	v_fma_f32 v111, -v101, v107, 1.0
	v_mul_f32_e32 v110, v100, v106
	v_fma_f32 v113, -v29, v109, v98
	v_fmac_f32_e32 v107, v111, v107
	v_fma_f32 v114, -v99, v110, v100
	v_fmac_f32_e32 v109, v113, v105
	v_fma_f32 v112, -v103, v108, 1.0
	v_mul_f32_e32 v111, v102, v107
	v_fmac_f32_e32 v110, v114, v106
	v_fma_f32 v29, -v29, v109, v98
	v_div_scale_f32 v104, s[10:11], s16, v33, s16
	v_fmac_f32_e32 v108, v112, v108
	v_fma_f32 v115, -v101, v111, v102
	v_fma_f32 v98, -v99, v110, v100
	v_div_fmas_f32 v29, v29, v105, v109
	s_mov_b64 vcc, s[6:7]
	v_mul_f32_e32 v112, v104, v108
	v_fmac_f32_e32 v111, v115, v107
	v_div_fixup_f32 v29, v29, v30, s16
	v_div_fmas_f32 v98, v98, v106, v110
	v_cmp_lt_f32_e32 vcc, 0, v30
	v_fma_f32 v116, -v103, v112, v104
	v_fma_f32 v99, -v101, v111, v102
	v_cndmask_b32_e32 v29, 0, v29, vcc
	s_mov_b64 vcc, s[8:9]
	v_fmac_f32_e32 v112, v116, v108
	v_div_fixup_f32 v30, v98, v31, s16
	v_div_fmas_f32 v98, v99, v107, v111
	v_cmp_lt_f32_e32 vcc, 0, v31
	v_fma_f32 v100, -v103, v112, v104
	v_div_fixup_f32 v31, v98, v32, s16
	v_cndmask_b32_e32 v30, 0, v30, vcc
	s_mov_b64 vcc, s[10:11]
	v_div_fmas_f32 v98, v100, v108, v112
	v_cmp_lt_f32_e32 vcc, 0, v32
	v_div_fixup_f32 v32, v98, v33, s16
	s_waitcnt vmcnt(0) lgkmcnt(0)
	v_mul_f32_e32 v34, v34, v29
	v_mul_f32_e32 v38, v29, v38
	v_mul_f32_e32 v42, v29, v42
	v_mul_f32_e32 v46, v29, v46
	v_mul_f32_e32 v50, v29, v50
	v_mul_f32_e32 v54, v29, v54
	v_mul_f32_e32 v58, v29, v58
	v_mul_f32_e32 v62, v29, v62
	v_mul_f32_e32 v66, v29, v66
	v_mul_f32_e32 v70, v29, v70
	v_mul_f32_e32 v74, v29, v74
	v_mul_f32_e32 v78, v29, v78
	v_mul_f32_e32 v82, v29, v82
	v_mul_f32_e32 v86, v29, v86
	v_cndmask_b32_e32 v31, 0, v31, vcc
	v_med3_f32 v34, v34, s34, v20
	v_med3_f32 v38, v38, s34, v20
	v_med3_f32 v42, v42, s34, v20
	v_med3_f32 v46, v46, s34, v20
	v_mul_f32_e32 v39, v30, v39
	v_mul_f32_e32 v43, v30, v43
	v_mul_f32_e32 v47, v30, v47
	v_med3_f32 v50, v50, s34, v20
	v_med3_f32 v54, v54, s34, v20
	v_mul_f32_e32 v55, v30, v55
	v_cmp_lt_f32_e32 vcc, 0, v33
	v_mul_f32_e32 v90, v29, v90
	v_mul_f32_e32 v35, v35, v30
	v_med3_f32 v58, v58, s34, v20
	v_med3_f32 v62, v62, s34, v20
	v_mul_f32_e32 v51, v30, v51
	v_mul_f32_e32 v59, v30, v59
	v_mul_f32_e32 v63, v30, v63
	v_med3_f32 v66, v66, s34, v20
	v_med3_f32 v70, v70, s34, v20
	v_med3_f32 v74, v74, s34, v20
	v_med3_f32 v78, v78, s34, v20
	v_mul_f32_e32 v71, v30, v71
	v_mul_f32_e32 v79, v30, v79
	v_med3_f32 v82, v82, s34, v20
	v_med3_f32 v86, v86, s34, v20
	v_mul_f32_e32 v87, v30, v87
	v_cndmask_b32_e32 v32, 0, v32, vcc
	v_rndne_f32_e32 v33, v34
	v_rndne_f32_e32 v34, v38
	v_rndne_f32_e32 v38, v42
	v_rndne_f32_e32 v42, v46
	v_med3_f32 v39, v39, s34, v20
	v_med3_f32 v43, v43, s34, v20
	v_med3_f32 v46, v47, s34, v20
	v_mul_f32_e32 v40, v31, v40
	v_mul_f32_e32 v47, v31, v48
	v_rndne_f32_e32 v48, v50
	v_rndne_f32_e32 v50, v54
	v_med3_f32 v55, v55, s34, v20
	v_mul_f32_e32 v56, v31, v56
	v_mul_f32_e32 v29, v29, v94
	v_mul_f32_e32 v67, v30, v67
	v_mul_f32_e32 v75, v30, v75
	v_med3_f32 v90, v90, s34, v20
	v_mul_f32_e32 v83, v30, v83
	v_mul_f32_e32 v91, v30, v91
	v_med3_f32 v35, v35, s34, v20
	v_mul_f32_e32 v36, v36, v31
	v_mul_f32_e32 v44, v31, v44
	v_rndne_f32_e32 v54, v58
	v_rndne_f32_e32 v58, v62
	v_med3_f32 v51, v51, s34, v20
	v_med3_f32 v59, v59, s34, v20
	v_med3_f32 v62, v63, s34, v20
	v_mul_f32_e32 v52, v31, v52
	v_mul_f32_e32 v60, v31, v60
	v_mul_f32_e32 v63, v31, v64
	v_rndne_f32_e32 v64, v66
	v_rndne_f32_e32 v66, v70
	v_rndne_f32_e32 v70, v74
	v_rndne_f32_e32 v74, v78
	v_med3_f32 v71, v71, s34, v20
	v_med3_f32 v78, v79, s34, v20
	v_mul_f32_e32 v72, v31, v72
	v_mul_f32_e32 v79, v31, v80
	v_rndne_f32_e32 v80, v82
	v_rndne_f32_e32 v82, v86
	v_med3_f32 v87, v87, s34, v20
	v_mul_f32_e32 v88, v31, v88
	v_cvt_i32_f32_e32 v34, v34
	v_rndne_f32_e32 v39, v39
	v_rndne_f32_e32 v43, v43
	v_med3_f32 v40, v40, s34, v20
	v_mul_f32_e32 v41, v32, v41
	v_cvt_i32_f32_e32 v50, v50
	v_rndne_f32_e32 v55, v55
	v_med3_f32 v56, v56, s34, v20
	v_mul_f32_e32 v57, v32, v57
	v_med3_f32 v29, v29, s34, v20
	v_mul_f32_e32 v30, v30, v95
	v_med3_f32 v67, v67, s34, v20
	v_med3_f32 v75, v75, s34, v20
	v_mul_f32_e32 v68, v31, v68
	v_mul_f32_e32 v76, v31, v76
	v_rndne_f32_e32 v86, v90
	v_med3_f32 v83, v83, s34, v20
	v_med3_f32 v90, v91, s34, v20
	v_mul_f32_e32 v84, v31, v84
	v_mul_f32_e32 v91, v31, v92
	v_cvt_i32_f32_e32 v33, v33
	v_cvt_i32_f32_sdwa v38, v38 dst_sel:WORD_1 dst_unused:UNUSED_PAD src0_sel:DWORD
	v_rndne_f32_e32 v35, v35
	v_med3_f32 v36, v36, s34, v20
	v_med3_f32 v44, v44, s34, v20
	v_mul_f32_e32 v37, v37, v32
	v_mul_f32_e32 v45, v32, v45
	v_cvt_i32_f32_e32 v48, v48
	v_cvt_i32_f32_sdwa v54, v54 dst_sel:WORD_1 dst_unused:UNUSED_PAD src0_sel:DWORD
	v_rndne_f32_e32 v51, v51
	v_rndne_f32_e32 v59, v59
	v_med3_f32 v52, v52, s34, v20
	v_med3_f32 v60, v60, s34, v20
	v_mul_f32_e32 v53, v32, v53
	v_mul_f32_e32 v61, v32, v61
	v_cvt_i32_f32_e32 v66, v66
	v_rndne_f32_e32 v71, v71
	v_med3_f32 v72, v72, s34, v20
; __device__ __forceinline__ unsigned pack_i8x4(float a, float b, float c, float d) {
;     const int ia = (int)rintf(fminf(fmaxf(a, -127.f), 127.f)), ib = (int)rintf(fminf(fmaxf(b, -127.f), 127.f)), ic = (int)rintf(fminf(fmaxf(c, -127.f), 127.f)), id = (int)rintf(fminf(fmaxf(d, -127.f), 127.f));
;     return (unsigned)(ia & 0xff) | ((unsigned)(ib & 0xff) << 8) | ((unsigned)(ic & 0xff) << 16) | ((unsigned)(id & 0xff) << 24);
; __device__ __forceinline__ void cvt_item_i8(const float* src, int ld, int k0, int c0, unsigned char* dst, int Kd, int drow0, const float* cmx  , unsigned char* scr, int lane) {
;     ...
; #pragma unroll
;     for (int g = 0; g < 4; ++g)
; #pragma unroll
;         for (int i = 0; i < 4; ++i) *(unsigned*)(scr + (4 * c + i) * 132 + 32 * g + 4 * q) = pack_i8x4(v[g][0][i] * inv[i], v[g][1][i] * inv[i], v[g][2][i] * inv[i], v[g][3][i] * inv[i]);
	v_mul_f32_e32 v73, v32, v73
	v_cvt_i32_f32_e32 v82, v82
	v_rndne_f32_e32 v87, v87
	v_med3_f32 v88, v88, s34, v20
	v_mul_f32_e32 v89, v32, v89
	v_cvt_i32_f32_e32 v39, v39
	v_cvt_i32_f32_sdwa v43, v43 dst_sel:WORD_1 dst_unused:UNUSED_PAD src0_sel:DWORD
	v_rndne_f32_e32 v40, v40
	v_med3_f32 v41, v41, s34, v20
	v_cvt_i32_f32_e32 v55, v55
	v_rndne_f32_e32 v56, v56
	v_med3_f32 v57, v57, s34, v20
	v_rndne_f32_e32 v29, v29
	v_med3_f32 v30, v30, s34, v20
	v_mul_f32_e32 v31, v31, v96
	v_cvt_i32_f32_sdwa v42, v42 dst_sel:BYTE_3 dst_unused:UNUSED_PAD src0_sel:DWORD
	v_rndne_f32_e32 v46, v46
	v_med3_f32 v47, v47, s34, v20
	v_mul_f32_e32 v49, v32, v49
	v_cvt_i32_f32_sdwa v58, v58 dst_sel:BYTE_3 dst_unused:UNUSED_PAD src0_sel:DWORD
	v_rndne_f32_e32 v62, v62
	v_med3_f32 v63, v63, s34, v20
	v_mul_f32_e32 v65, v32, v65
	v_cvt_i32_f32_e32 v64, v64
	v_cvt_i32_f32_sdwa v70, v70 dst_sel:WORD_1 dst_unused:UNUSED_PAD src0_sel:DWORD
	v_rndne_f32_e32 v67, v67
	v_rndne_f32_e32 v75, v75
	v_med3_f32 v68, v68, s34, v20
	v_med3_f32 v76, v76, s34, v20
	v_mul_f32_e32 v69, v32, v69
	v_mul_f32_e32 v77, v32, v77
	v_cvt_i32_f32_e32 v80, v80
	v_cvt_i32_f32_sdwa v86, v86 dst_sel:WORD_1 dst_unused:UNUSED_PAD src0_sel:DWORD
	v_rndne_f32_e32 v83, v83
	v_rndne_f32_e32 v90, v90
	v_med3_f32 v84, v84, s34, v20
	v_med3_f32 v91, v91, s34, v20
	v_mul_f32_e32 v85, v32, v85
	v_mul_f32_e32 v92, v32, v93
	v_cvt_i32_f32_e32 v35, v35
	v_rndne_f32_e32 v36, v36
	v_rndne_f32_e32 v44, v44
	v_med3_f32 v37, v37, s34, v20
	v_med3_f32 v45, v45, s34, v20
	v_cvt_i32_f32_e32 v51, v51
	v_cvt_i32_f32_sdwa v59, v59 dst_sel:WORD_1 dst_unused:UNUSED_PAD src0_sel:DWORD
	v_rndne_f32_e32 v52, v52
	v_rndne_f32_e32 v60, v60
	v_med3_f32 v53, v53, s34, v20
	v_med3_f32 v61, v61, s34, v20
	v_cvt_i32_f32_e32 v71, v71
	v_rndne_f32_e32 v72, v72
	v_med3_f32 v73, v73, s34, v20
	v_cvt_i32_f32_e32 v87, v87
	v_rndne_f32_e32 v88, v88
	v_med3_f32 v89, v89, s34, v20
	v_cvt_i32_f32_e32 v40, v40
	v_rndne_f32_e32 v41, v41
	v_cvt_i32_f32_e32 v56, v56
	v_rndne_f32_e32 v57, v57
	v_cvt_i32_f32_sdwa v74, v74 dst_sel:BYTE_3 dst_unused:UNUSED_PAD src0_sel:DWORD
	v_rndne_f32_e32 v78, v78
	v_med3_f32 v79, v79, s34, v20
	v_mul_f32_e32 v81, v32, v81
	v_cvt_i32_f32_sdwa v29, v29 dst_sel:BYTE_3 dst_unused:UNUSED_PAD src0_sel:DWORD
	v_rndne_f32_e32 v30, v30
	v_med3_f32 v31, v31, s34, v20
	v_mul_f32_e32 v32, v32, v97
	v_cvt_i32_f32_sdwa v46, v46 dst_sel:BYTE_3 dst_unused:UNUSED_PAD src0_sel:DWORD
	v_rndne_f32_e32 v47, v47
	v_med3_f32 v49, v49, s34, v20
	v_cvt_i32_f32_sdwa v62, v62 dst_sel:BYTE_3 dst_unused:UNUSED_PAD src0_sel:DWORD
	v_rndne_f32_e32 v63, v63
	v_med3_f32 v65, v65, s34, v20
	v_cvt_i32_f32_e32 v67, v67
	v_cvt_i32_f32_sdwa v75, v75 dst_sel:WORD_1 dst_unused:UNUSED_PAD src0_sel:DWORD
	v_rndne_f32_e32 v68, v68
	v_rndne_f32_e32 v76, v76
	v_med3_f32 v69, v69, s34, v20
	v_med3_f32 v77, v77, s34, v20
	v_cvt_i32_f32_e32 v83, v83
	v_cvt_i32_f32_sdwa v90, v90 dst_sel:WORD_1 dst_unused:UNUSED_PAD src0_sel:DWORD
	v_rndne_f32_e32 v84, v84
	v_rndne_f32_e32 v91, v91
	v_med3_f32 v85, v85, s34, v20
	v_med3_f32 v92, v92, s34, v20
	v_cvt_i32_f32_e32 v36, v36
	v_cvt_i32_f32_sdwa v44, v44 dst_sel:WORD_1 dst_unused:UNUSED_PAD src0_sel:DWORD
	v_rndne_f32_e32 v37, v37
	v_rndne_f32_e32 v45, v45
	v_cvt_i32_f32_e32 v52, v52
	v_cvt_i32_f32_sdwa v60, v60 dst_sel:WORD_1 dst_unused:UNUSED_PAD src0_sel:DWORD
	v_rndne_f32_e32 v53, v53
	v_rndne_f32_e32 v61, v61
	v_cvt_i32_f32_e32 v72, v72
	v_rndne_f32_e32 v73, v73
	v_cvt_i32_f32_e32 v88, v88
	v_rndne_f32_e32 v89, v89
	v_cvt_i32_f32_e32 v41, v41
	v_cvt_i32_f32_e32 v57, v57
	v_cvt_i32_f32_sdwa v78, v78 dst_sel:BYTE_3 dst_unused:UNUSED_PAD src0_sel:DWORD
	v_rndne_f32_e32 v79, v79
	v_med3_f32 v81, v81, s34, v20
	v_cvt_i32_f32_sdwa v30, v30 dst_sel:BYTE_3 dst_unused:UNUSED_PAD src0_sel:DWORD
	v_rndne_f32_e32 v31, v31
	v_med3_f32 v32, v32, s34, v20
	v_cvt_i32_f32_sdwa v47, v47 dst_sel:BYTE_3 dst_unused:UNUSED_PAD src0_sel:DWORD
	v_rndne_f32_e32 v49, v49
	v_cvt_i32_f32_sdwa v63, v63 dst_sel:BYTE_3 dst_unused:UNUSED_PAD src0_sel:DWORD
	v_rndne_f32_e32 v65, v65
	v_cvt_i32_f32_e32 v68, v68
	v_cvt_i32_f32_sdwa v76, v76 dst_sel:WORD_1 dst_unused:UNUSED_PAD src0_sel:DWORD
	v_rndne_f32_e32 v69, v69
	v_rndne_f32_e32 v77, v77
	v_cvt_i32_f32_e32 v84, v84
; __device__ __forceinline__ void cvt_item_i8(const float* src, int ld, int k0, int c0, unsigned char* dst, int Kd, int drow0, const float* cmx  , unsigned char* scr, int lane) {
;     ...
; #pragma unroll
;     for (int g = 0; g < 4; ++g)
; #pragma unroll
;         for (int i = 0; i < 4; ++i) *(unsigned*)(scr + (4 * c + i) * 132 + 32 * g + 4 * q) = pack_i8x4(v[g][0][i] * inv[i], v[g][1][i] * inv[i], v[g][2][i] * inv[i], v[g][3][i] * inv[i]);
;     asm volatile("s_waitcnt lgkmcnt(0)" ::: "memory");
; #pragma unroll
;     for (int r = 0; r < 4; ++r) { const int n = 8 * r + (lane >> 3), ch = lane & 7; const unsigned char* p = scr + n * 132 + ch * 16;
;         u32x4 o; o.x = *(const unsigned*)(p); o.y = *(const unsigned*)(p + 4); o.z = *(const unsigned*)(p + 8); o.w = *(const unsigned*)(p + 12);
;         *(u32x4*)(dst + (size_t)(drow0 + n) * Kd + k0 + 16 * ch) = o; }
;     asm volatile("s_waitcnt lgkmcnt(0)" ::: "memory");
	v_cvt_i32_f32_sdwa v91, v91 dst_sel:WORD_1 dst_unused:UNUSED_PAD src0_sel:DWORD
	v_rndne_f32_e32 v85, v85
	v_rndne_f32_e32 v92, v92
	v_cvt_i32_f32_e32 v37, v37
	v_cvt_i32_f32_sdwa v45, v45 dst_sel:WORD_1 dst_unused:UNUSED_PAD src0_sel:DWORD
	v_cvt_i32_f32_e32 v53, v53
	v_cvt_i32_f32_sdwa v61, v61 dst_sel:WORD_1 dst_unused:UNUSED_PAD src0_sel:DWORD
	v_cvt_i32_f32_e32 v73, v73
	v_cvt_i32_f32_e32 v89, v89
	v_lshlrev_b32_e32 v34, 8, v34
	v_lshlrev_b32_e32 v50, 8, v50
	v_cvt_i32_f32_sdwa v79, v79 dst_sel:BYTE_3 dst_unused:UNUSED_PAD src0_sel:DWORD
	v_rndne_f32_e32 v81, v81
	v_cvt_i32_f32_sdwa v31, v31 dst_sel:BYTE_3 dst_unused:UNUSED_PAD src0_sel:DWORD
	v_rndne_f32_e32 v32, v32
	v_cvt_i32_f32_sdwa v49, v49 dst_sel:BYTE_3 dst_unused:UNUSED_PAD src0_sel:DWORD
	v_cvt_i32_f32_sdwa v65, v65 dst_sel:BYTE_3 dst_unused:UNUSED_PAD src0_sel:DWORD
	v_cvt_i32_f32_e32 v69, v69
	v_cvt_i32_f32_sdwa v77, v77 dst_sel:WORD_1 dst_unused:UNUSED_PAD src0_sel:DWORD
	v_cvt_i32_f32_e32 v85, v85
	v_cvt_i32_f32_sdwa v92, v92 dst_sel:WORD_1 dst_unused:UNUSED_PAD src0_sel:DWORD
	v_and_b32_e32 v38, 0xff0000, v38
	v_and_b32_e32 v54, 0xff0000, v54
	v_lshlrev_b32_e32 v66, 8, v66
	v_lshlrev_b32_e32 v82, 8, v82
	v_perm_b32 v33, v34, v33, s35
	v_lshlrev_b32_e32 v34, 8, v39
	v_and_b32_e32 v39, 0xff0000, v43
	v_perm_b32 v43, v50, v48, s35
	v_lshlrev_b32_e32 v48, 8, v55
	v_cvt_i32_f32_sdwa v81, v81 dst_sel:BYTE_3 dst_unused:UNUSED_PAD src0_sel:DWORD
	v_cvt_i32_f32_sdwa v32, v32 dst_sel:BYTE_3 dst_unused:UNUSED_PAD src0_sel:DWORD
	v_and_b32_e32 v70, 0xff0000, v70
	v_and_b32_e32 v86, 0xff0000, v86
	v_and_b32_e32 v50, 0xff0000, v59
	v_perm_b32 v55, v66, v64, s35
	v_lshlrev_b32_e32 v59, 8, v71
	v_perm_b32 v66, v82, v80, s35
	v_lshlrev_b32_e32 v71, 8, v87
	v_or3_b32 v33, v33, v38, v42
	v_perm_b32 v34, v34, v35, s35
	v_lshlrev_b32_e32 v35, 8, v40
	v_or3_b32 v40, v43, v54, v58
	v_perm_b32 v42, v48, v51, s35
	v_lshlrev_b32_e32 v43, 8, v56
	v_and_b32_e32 v64, 0xff0000, v75
	v_and_b32_e32 v75, 0xff0000, v90
	v_and_b32_e32 v38, 0xff0000, v44
	v_and_b32_e32 v44, 0xff0000, v60
	v_or3_b32 v48, v55, v70, v74
	v_perm_b32 v51, v59, v67, s35
	v_lshlrev_b32_e32 v54, 8, v72
	v_or3_b32 v29, v66, v86, v29
	v_perm_b32 v56, v71, v83, s35
	v_lshlrev_b32_e32 v58, 8, v88
	v_or3_b32 v34, v34, v39, v46
	v_perm_b32 v35, v35, v36, s35
	v_lshlrev_b32_e32 v36, 8, v41
	ds_write2_b32 v21, v33, v40 offset1:8
	v_or3_b32 v33, v42, v50, v62
	v_perm_b32 v40, v43, v52, s35
	v_lshlrev_b32_e32 v41, 8, v57
	v_and_b32_e32 v55, 0xff0000, v76
	v_and_b32_e32 v59, 0xff0000, v91
	v_and_b32_e32 v39, 0xff0000, v45
	v_and_b32_e32 v42, 0xff0000, v61
	v_or3_b32 v43, v51, v64, v78
	v_perm_b32 v45, v54, v68, s35
	v_lshlrev_b32_e32 v46, 8, v73
	ds_write2_b32 v21, v48, v29 offset0:16 offset1:24
	v_or3_b32 v29, v56, v75, v30
	v_perm_b32 v30, v58, v84, s35
	v_lshlrev_b32_e32 v48, 8, v89
	v_or3_b32 v35, v35, v38, v47
	v_perm_b32 v36, v36, v37, s35
	ds_write2_b32 v21, v34, v33 offset0:33 offset1:41
	v_or3_b32 v33, v40, v44, v63
	v_perm_b32 v34, v41, v53, s35
	v_and_b32_e32 v50, 0xff0000, v77
	v_and_b32_e32 v51, 0xff0000, v92
	v_or3_b32 v37, v45, v55, v79
	v_perm_b32 v38, v46, v69, s35
	ds_write2_b32 v21, v43, v29 offset0:49 offset1:57
	v_or3_b32 v29, v30, v59, v31
	v_perm_b32 v30, v48, v85, s35
	v_or3_b32 v31, v36, v39, v49
	ds_write2_b32 v21, v35, v33 offset0:66 offset1:74
	v_or3_b32 v33, v34, v42, v65
	v_or3_b32 v34, v38, v50, v81
	ds_write2_b32 v21, v37, v29 offset0:82 offset1:90
	v_or3_b32 v29, v30, v51, v32
	ds_write2_b32 v21, v31, v33 offset0:99 offset1:107
	ds_write2_b32 v21, v34, v29 offset0:115 offset1:123
	s_waitcnt lgkmcnt(0)
	ds_read2_b32 v[30:31], v22 offset1:1
	ds_read2_b32 v[32:33], v22 offset0:2 offset1:3
	ds_read2_b32 v[34:35], v23 offset1:1
	ds_read2_b32 v[36:37], v24 offset1:1
	ds_read2_b32 v[38:39], v25 offset1:1
	ds_read2_b32 v[40:41], v26 offset1:1
	ds_read2_b32 v[42:43], v27 offset1:1
	ds_read2_b32 v[44:45], v28 offset1:1
	s_waitcnt lgkmcnt(6)
	global_store_dwordx4 v[10:11], v[30:33], off
	s_waitcnt lgkmcnt(4)
	global_store_dwordx4 v[12:13], v[34:37], off
	s_waitcnt lgkmcnt(2)
	global_store_dwordx4 v[14:15], v[38:41], off
	s_waitcnt lgkmcnt(0)
	global_store_dwordx4 v[6:7], v[42:45], off
	s_waitcnt lgkmcnt(0)
	s_cbranch_scc1 .LBB0_1672

; __device__ __forceinline__ void cvt_item_i8(const float* src, int ld, int k0, int c0, unsigned char* dst, int Kd, int drow0, const float* cmx  , unsigned char* scr, int lane) {
;     const int c = lane & 7, q = lane >> 3;
;     const f32x4 cm = *(const f32x4*)(cmx + 4 * c);
;     f32x4 inv; inv[0] = cm[0] > 0.f ? 127.f / cm[0] : 0.f; inv[1] = cm[1] > 0.f ? 127.f / cm[1] : 0.f; inv[2] = cm[2] > 0.f ? 127.f / cm[2] : 0.f; inv[3] = cm[3] > 0.f ? 127.f / cm[3] : 0.f;
;     f32x4 v[4][4];
; #pragma unroll
;     for (int g = 0; g < 4; ++g)
; #pragma unroll
;         for (int j = 0; j < 4; ++j) v[g][j] = __builtin_nontemporal_load((const f32x4*)(src + (size_t)(k0 + 32 * g + 4 * q + j) * ld + c0 + 4 * c));
; template <int GRP>
; __device__ __forceinline__ void conv_item(Frame& F, int r) {
;     ...
;     else { constexpr int KBN = (GRP == 3) ? 16 : CMS_KB, I_E = KBN * 88; const int up = r / (8 * I_E); r %= (8 * I_E); const int e = r / I_E; r %= I_E; const int kb = r / 88, nb = r % 88, n0 = nb * 32, drow = (n0 >> 7) * 256 + up * 128 + (n0 & 127);
;         if (GRP == 3) cvt_item_i8(inptr(F, up ? IN_MU : IN_MG) + (size_t)e * D * DFE, DFE, kb * 128, n0, ws + WS_MGU + (size_t)e * 2 * DFE * D, D, drow, cmx + 2 * DFF + e * 2 * DFE + drow, scr, F.lane);
;     ...
;     for (int it = first + F.gw; it < N; it += F.NGW) conv_item<GRP>(F, it);
.LBB0_1909:
	s_mul_hi_i32 s0, s3, 0x2e8ba2e9
	s_lshr_b32 s1, s0, 31
	s_ashr_i32 s0, s0, 11
	s_add_i32 s0, s0, s1
	s_mul_i32 s1, s0, 0xffffd400
	s_lshl_b32 s6, s0, 7
	s_add_i32 s0, s3, s1
	s_mul_i32 s1, s0, 0xba3
	s_lshr_b32 s7, s1, 31
	s_ashr_i32 s1, s1, 22
	s_add_i32 s1, s1, s7
	s_mul_i32 s7, s1, 0x580
	s_sub_i32 s0, s0, s7
	s_sext_i32_i16 s38, s0
	s_mulk_i32 s38, 0xba3
	s_lshr_b32 s40, s38, 31
	s_ashr_i32 s38, s38, 18
	s_add_i32 s40, s38, s40
	s_sext_i32_i16 s38, s40
	s_mulk_i32 s40, 0x58
	s_sub_i32 s0, s0, s40
	s_sext_i32_i16 s40, s0
	s_lshl_b32 s0, s40, 5
	s_lshl_b32 s40, s40, 6
	s_and_b32 s40, s40, 0xffffff00
	s_and_b32 s41, s0, 0x60
	s_add_i32 s40, s40, s6
	s_add_i32 s39, s3, 0x2bff
	s_or_b32 s6, s40, s41
	s_cmpk_lt_u32 s39, 0x57ff
	s_cselect_b32 s39, s15, 0xa8
	v_or_b32_e32 v8, s6, v17
	s_add_i32 s39, s39, 0
	v_ashrrev_i32_e32 v9, 31, v8
	s_add_i32 s39, s39, 0x20200
	v_lshlrev_b64 v[98:99], 11, v[8:9]
	v_mov_b32_e32 v8, s39
	ds_read_b64 v[8:9], v8
	s_sext_i32_i16 s11, s1
	s_mul_i32 s9, s11, 0x1600000
	s_mul_hi_i32 s1, s11, 0x1600000
	s_mul_i32 s10, s11, 0xb00000
	s_waitcnt lgkmcnt(0)
	v_readfirstlane_b32 s39, v8
	v_readfirstlane_b32 s40, v9
	s_add_u32 s9, s39, s9
	s_addc_u32 s39, s40, s1
	s_lshl_b32 s38, s38, 7
	s_mul_hi_i32 s7, s11, 0xb00000
	s_add_u32 s10, s4, s10
	s_mul_hi_i32 s8, s11, 0x5800
	s_mulk_i32 s11, 0x5800
	s_addc_u32 s40, s12, s7
	s_add_u32 s1, s13, s11
	s_addc_u32 s8, s14, s8
	s_ashr_i32 s7, s6, 31
	v_or_b32_e32 v6, s6, v1
	v_or_b32_e32 v10, s6, v18
	v_or_b32_e32 v12, s6, v19
	s_lshl_b64 s[6:7], s[6:7], 2
	s_add_u32 s6, s1, s6
	s_addc_u32 s7, s8, s7
	s_ashr_i32 s1, s0, 31
	s_lshl_b64 s[0:1], s[0:1], 2
	v_or_b32_e32 v8, s38, v16
	s_add_u32 s0, s9, s0
	v_ashrrev_i32_e32 v11, 31, v10
	v_mul_i32_i24_e32 v8, 0x2c00, v8
	s_addc_u32 s1, s39, s1
	v_lshlrev_b64 v[100:101], 11, v[10:11]
	v_ashrrev_i32_e32 v9, 31, v8
	v_lshl_add_u64 v[10:11], s[0:1], 0, v[4:5]
	v_ashrrev_i32_e32 v7, 31, v6
	v_ashrrev_i32_e32 v13, 31, v12
	v_lshl_add_u64 v[10:11], v[10:11], 0, v[8:9]
	v_lshlrev_b64 v[14:15], 11, v[6:7]
	v_lshlrev_b64 v[6:7], 11, v[12:13]
	v_add_co_u32_e32 v12, vcc, s17, v10
	global_load_dwordx4 v[30:33], v4, s[6:7]
	s_nop 0
	v_addc_co_u32_e32 v13, vcc, 0, v11, vcc
	v_add_co_u32_e32 v42, vcc, s20, v10
	s_ashr_i32 s6, s38, 31
	s_nop 0
	v_addc_co_u32_e32 v43, vcc, 0, v11, vcc
	v_add_co_u32_e32 v46, vcc, s21, v10
	s_add_u32 s0, s10, s38
	s_nop 0
	v_addc_co_u32_e32 v47, vcc, 0, v11, vcc
	v_add_co_u32_e32 v50, vcc, s22, v10
	s_addc_u32 s1, s40, s6
	s_nop 0
	v_addc_co_u32_e32 v51, vcc, 0, v11, vcc
	v_add_co_u32_e32 v54, vcc, s23, v10
	v_lshl_add_u64 v[8:9], s[0:1], 0, v[2:3]
	s_nop 0
	v_addc_co_u32_e32 v55, vcc, 0, v11, vcc
	v_add_co_u32_e32 v58, vcc, s24, v10
	v_lshl_add_u64 v[6:7], v[8:9], 0, v[6:7]
	s_nop 0
	v_addc_co_u32_e32 v59, vcc, 0, v11, vcc
	v_add_co_u32_e32 v62, vcc, s25, v10
	s_add_i32 s3, s3, s42
	s_nop 0
	v_addc_co_u32_e32 v63, vcc, 0, v11, vcc
	v_add_co_u32_e32 v66, vcc, s26, v10
	s_cmpk_lt_i32 s3, 0x5800
	s_nop 0
	v_addc_co_u32_e32 v67, vcc, 0, v11, vcc
	v_add_co_u32_e32 v70, vcc, s27, v10
	s_nop 0
	s_nop 0
	v_addc_co_u32_e32 v71, vcc, 0, v11, vcc
	v_add_co_u32_e32 v74, vcc, s28, v10
	s_nop 0
	s_nop 0
	v_addc_co_u32_e32 v75, vcc, 0, v11, vcc
	v_add_co_u32_e32 v78, vcc, s29, v10
	s_nop 0
	s_nop 0
	v_addc_co_u32_e32 v79, vcc, 0, v11, vcc
	v_add_co_u32_e32 v82, vcc, s30, v10
	s_nop 0
	s_nop 0
	v_addc_co_u32_e32 v83, vcc, 0, v11, vcc
	v_add_co_u32_e32 v86, vcc, s31, v10
	s_nop 0
	s_nop 0
	v_addc_co_u32_e32 v87, vcc, 0, v11, vcc
	v_add_co_u32_e32 v90, vcc, s34, v10
	s_nop 0
	s_nop 0
	v_addc_co_u32_e32 v91, vcc, 0, v11, vcc
	v_add_co_u32_e32 v94, vcc, s35, v10
	s_nop 0
	s_nop 0
	v_addc_co_u32_e32 v95, vcc, 0, v11, vcc
	global_load_dwordx4 v[34:37], v[10:11], off nt
	global_load_dwordx4 v[38:41], v[12:13], off offset:3072 nt
	s_nop 0
	global_load_dwordx4 v[42:45], v[42:43], off offset:2048 nt
	s_nop 0
	global_load_dwordx4 v[46:49], v[46:47], off offset:1024 nt
	s_nop 0
	global_load_dwordx4 v[50:53], v[50:51], off nt
	s_nop 0
	global_load_dwordx4 v[54:57], v[54:55], off offset:3072 nt
	s_nop 0
	global_load_dwordx4 v[58:61], v[58:59], off offset:2048 nt
	s_nop 0
	global_load_dwordx4 v[62:65], v[62:63], off offset:1024 nt
	s_nop 0
	global_load_dwordx4 v[66:69], v[66:67], off nt
	s_nop 0
	global_load_dwordx4 v[70:73], v[70:71], off offset:3072 nt
	s_nop 0
	global_load_dwordx4 v[74:77], v[74:75], off offset:2048 nt
	s_nop 0
	global_load_dwordx4 v[78:81], v[78:79], off offset:1024 nt
	s_nop 0
	global_load_dwordx4 v[82:85], v[82:83], off nt
	s_nop 0
	global_load_dwordx4 v[86:89], v[86:87], off offset:3072 nt
	s_nop 0
	global_load_dwordx4 v[90:93], v[90:91], off offset:2048 nt
	s_nop 0
	global_load_dwordx4 v[94:97], v[94:95], off offset:1024 nt
	s_waitcnt vmcnt(16)
; __device__ __forceinline__ unsigned pack_i8x4(float a, float b, float c, float d) {
;     const int ia = (int)rintf(fminf(fmaxf(a, -127.f), 127.f)), ib = (int)rintf(fminf(fmaxf(b, -127.f), 127.f)), ic = (int)rintf(fminf(fmaxf(c, -127.f), 127.f)), id = (int)rintf(fminf(fmaxf(d, -127.f), 127.f));
;     return (unsigned)(ia & 0xff) | ((unsigned)(ib & 0xff) << 8) | ((unsigned)(ic & 0xff) << 16) | ((unsigned)(id & 0xff) << 24);
; __device__ __forceinline__ void cvt_item_i8(const float* src, int ld, int k0, int c0, unsigned char* dst, int Kd, int drow0, const float* cmx  , unsigned char* scr, int lane) {
;     ...
;     f32x4 inv; inv[0] = cm[0] > 0.f ? 127.f / cm[0] : 0.f; inv[1] = cm[1] > 0.f ? 127.f / cm[1] : 0.f; inv[2] = cm[2] > 0.f ? 127.f / cm[2] : 0.f; inv[3] = cm[3] > 0.f ? 127.f / cm[3] : 0.f;
;     f32x4 v[4][4];
; #pragma unroll
;     for (int g = 0; g < 4; ++g)
; #pragma unroll
;         for (int j = 0; j < 4; ++j) v[g][j] = __builtin_nontemporal_load((const f32x4*)(src + (size_t)(k0 + 32 * g + 4 * q + j) * ld + c0 + 4 * c));
; #pragma unroll
;     for (int g = 0; g < 4; ++g)
; #pragma unroll
;         for (int i = 0; i < 4; ++i) *(unsigned*)(scr + (4 * c + i) * 132 + 32 * g + 4 * q) = pack_i8x4(v[g][0][i] * inv[i], v[g][1][i] * inv[i], v[g][2][i] * inv[i], v[g][3][i] * inv[i]);
	v_div_scale_f32 v29, s[0:1], v30, v30, s16
	v_rcp_f32_e32 v105, v29
	v_div_scale_f32 v103, s[0:1], v33, v33, s16
	v_fma_f32 v109, -v29, v105, 1.0
	v_rcp_f32_e32 v108, v103
	v_fmac_f32_e32 v105, v109, v105
	v_div_scale_f32 v102, s[8:9], s16, v32, s16
	v_lshl_add_u64 v[12:13], v[8:9], 0, v[98:99]
	v_div_scale_f32 v99, s[0:1], v31, v31, s16
	v_rcp_f32_e32 v106, v99
	v_lshl_add_u64 v[10:11], v[8:9], 0, v[14:15]
	v_lshl_add_u64 v[14:15], v[8:9], 0, v[100:101]
	v_div_scale_f32 v101, s[0:1], v32, v32, s16
	v_rcp_f32_e32 v107, v101
	v_div_scale_f32 v98, vcc, s16, v30, s16
	v_fma_f32 v110, -v99, v106, 1.0
	v_div_scale_f32 v100, s[6:7], s16, v31, s16
	v_fmac_f32_e32 v106, v110, v106
	v_mul_f32_e32 v109, v98, v105
	v_fma_f32 v111, -v101, v107, 1.0
	v_mul_f32_e32 v110, v100, v106
	v_fma_f32 v113, -v29, v109, v98
	v_fmac_f32_e32 v107, v111, v107
	v_fma_f32 v114, -v99, v110, v100
	v_fmac_f32_e32 v109, v113, v105
	v_fma_f32 v112, -v103, v108, 1.0
	v_mul_f32_e32 v111, v102, v107
	v_fmac_f32_e32 v110, v114, v106
	v_fma_f32 v29, -v29, v109, v98
	v_div_scale_f32 v104, s[10:11], s16, v33, s16
	v_fmac_f32_e32 v108, v112, v108
	v_fma_f32 v115, -v101, v111, v102
	v_fma_f32 v98, -v99, v110, v100
	v_div_fmas_f32 v29, v29, v105, v109
	s_mov_b64 vcc, s[6:7]
	v_mul_f32_e32 v112, v104, v108
	v_fmac_f32_e32 v111, v115, v107
	v_div_fixup_f32 v29, v29, v30, s16
	v_div_fmas_f32 v98, v98, v106, v110
	v_cmp_lt_f32_e32 vcc, 0, v30
	v_fma_f32 v116, -v103, v112, v104
	v_fma_f32 v99, -v101, v111, v102
	v_cndmask_b32_e32 v29, 0, v29, vcc
	s_mov_b64 vcc, s[8:9]
	v_fmac_f32_e32 v112, v116, v108
	v_div_fixup_f32 v30, v98, v31, s16
	v_div_fmas_f32 v98, v99, v107, v111
	v_cmp_lt_f32_e32 vcc, 0, v31
	v_fma_f32 v100, -v103, v112, v104
	v_div_fixup_f32 v31, v98, v32, s16
	v_cndmask_b32_e32 v30, 0, v30, vcc
	s_mov_b64 vcc, s[10:11]
	v_div_fmas_f32 v98, v100, v108, v112
	v_cmp_lt_f32_e32 vcc, 0, v32
	v_div_fixup_f32 v32, v98, v33, s16
	s_waitcnt vmcnt(0) lgkmcnt(0)
	v_mul_f32_e32 v34, v34, v29
	v_mul_f32_e32 v38, v29, v38
	v_mul_f32_e32 v42, v29, v42
	v_mul_f32_e32 v46, v29, v46
	v_mul_f32_e32 v50, v29, v50
	v_mul_f32_e32 v54, v29, v54
	v_mul_f32_e32 v58, v29, v58
	v_mul_f32_e32 v62, v29, v62
	v_mul_f32_e32 v66, v29, v66
	v_mul_f32_e32 v70, v29, v70
	v_mul_f32_e32 v74, v29, v74
	v_mul_f32_e32 v78, v29, v78
	v_mul_f32_e32 v82, v29, v82
	v_mul_f32_e32 v86, v29, v86
	v_cndmask_b32_e32 v31, 0, v31, vcc
	v_med3_f32 v34, v34, s36, v20
	v_med3_f32 v38, v38, s36, v20
	v_med3_f32 v42, v42, s36, v20
	v_med3_f32 v46, v46, s36, v20
	v_mul_f32_e32 v39, v30, v39
	v_mul_f32_e32 v43, v30, v43
	v_mul_f32_e32 v47, v30, v47
	v_med3_f32 v50, v50, s36, v20
	v_med3_f32 v54, v54, s36, v20
	v_mul_f32_e32 v55, v30, v55
	v_cmp_lt_f32_e32 vcc, 0, v33
	v_mul_f32_e32 v90, v29, v90
	v_mul_f32_e32 v35, v35, v30
	v_med3_f32 v58, v58, s36, v20
	v_med3_f32 v62, v62, s36, v20
	v_mul_f32_e32 v51, v30, v51
	v_mul_f32_e32 v59, v30, v59
	v_mul_f32_e32 v63, v30, v63
	v_med3_f32 v66, v66, s36, v20
	v_med3_f32 v70, v70, s36, v20
	v_med3_f32 v74, v74, s36, v20
	v_med3_f32 v78, v78, s36, v20
	v_mul_f32_e32 v71, v30, v71
	v_mul_f32_e32 v79, v30, v79
	v_med3_f32 v82, v82, s36, v20
	v_med3_f32 v86, v86, s36, v20
	v_mul_f32_e32 v87, v30, v87
	v_cndmask_b32_e32 v32, 0, v32, vcc
	v_rndne_f32_e32 v33, v34
	v_rndne_f32_e32 v34, v38
	v_rndne_f32_e32 v38, v42
	v_rndne_f32_e32 v42, v46
	v_med3_f32 v39, v39, s36, v20
	v_med3_f32 v43, v43, s36, v20
	v_med3_f32 v46, v47, s36, v20
	v_mul_f32_e32 v40, v31, v40
	v_mul_f32_e32 v47, v31, v48
	v_rndne_f32_e32 v48, v50
	v_rndne_f32_e32 v50, v54
	v_med3_f32 v55, v55, s36, v20
	v_mul_f32_e32 v56, v31, v56
	v_mul_f32_e32 v29, v29, v94
	v_mul_f32_e32 v67, v30, v67
	v_mul_f32_e32 v75, v30, v75
	v_med3_f32 v90, v90, s36, v20
	v_mul_f32_e32 v83, v30, v83
	v_mul_f32_e32 v91, v30, v91
	v_med3_f32 v35, v35, s36, v20
	v_mul_f32_e32 v36, v36, v31
	v_mul_f32_e32 v44, v31, v44
	v_rndne_f32_e32 v54, v58
	v_rndne_f32_e32 v58, v62
	v_med3_f32 v51, v51, s36, v20
	v_med3_f32 v59, v59, s36, v20
	v_med3_f32 v62, v63, s36, v20
	v_mul_f32_e32 v52, v31, v52
	v_mul_f32_e32 v60, v31, v60
	v_mul_f32_e32 v63, v31, v64
	v_rndne_f32_e32 v64, v66
	v_rndne_f32_e32 v66, v70
	v_rndne_f32_e32 v70, v74
	v_rndne_f32_e32 v74, v78
	v_med3_f32 v71, v71, s36, v20
	v_med3_f32 v78, v79, s36, v20
	v_mul_f32_e32 v72, v31, v72
	v_mul_f32_e32 v79, v31, v80
	v_rndne_f32_e32 v80, v82
	v_rndne_f32_e32 v82, v86
	v_med3_f32 v87, v87, s36, v20
	v_mul_f32_e32 v88, v31, v88
	v_cvt_i32_f32_e32 v34, v34
	v_rndne_f32_e32 v39, v39
	v_rndne_f32_e32 v43, v43
	v_med3_f32 v40, v40, s36, v20
	v_mul_f32_e32 v41, v32, v41
	v_cvt_i32_f32_e32 v50, v50
	v_rndne_f32_e32 v55, v55
	v_med3_f32 v56, v56, s36, v20
	v_mul_f32_e32 v57, v32, v57
	v_med3_f32 v29, v29, s36, v20
	v_mul_f32_e32 v30, v30, v95
	v_med3_f32 v67, v67, s36, v20
	v_med3_f32 v75, v75, s36, v20
	v_mul_f32_e32 v68, v31, v68
	v_mul_f32_e32 v76, v31, v76
	v_rndne_f32_e32 v86, v90
	v_med3_f32 v83, v83, s36, v20
	v_med3_f32 v90, v91, s36, v20
	v_mul_f32_e32 v84, v31, v84
	v_mul_f32_e32 v91, v31, v92
	v_cvt_i32_f32_e32 v33, v33
	v_cvt_i32_f32_sdwa v38, v38 dst_sel:WORD_1 dst_unused:UNUSED_PAD src0_sel:DWORD
	v_rndne_f32_e32 v35, v35
	v_med3_f32 v36, v36, s36, v20
	v_med3_f32 v44, v44, s36, v20
	v_mul_f32_e32 v37, v37, v32
	v_mul_f32_e32 v45, v32, v45
	v_cvt_i32_f32_e32 v48, v48
	v_cvt_i32_f32_sdwa v54, v54 dst_sel:WORD_1 dst_unused:UNUSED_PAD src0_sel:DWORD
	v_rndne_f32_e32 v51, v51
	v_rndne_f32_e32 v59, v59
	v_med3_f32 v52, v52, s36, v20
	v_med3_f32 v60, v60, s36, v20
	v_mul_f32_e32 v53, v32, v53
	v_mul_f32_e32 v61, v32, v61
	v_cvt_i32_f32_e32 v66, v66
	v_rndne_f32_e32 v71, v71
	v_med3_f32 v72, v72, s36, v20
; __device__ __forceinline__ unsigned pack_i8x4(float a, float b, float c, float d) {
;     const int ia = (int)rintf(fminf(fmaxf(a, -127.f), 127.f)), ib = (int)rintf(fminf(fmaxf(b, -127.f), 127.f)), ic = (int)rintf(fminf(fmaxf(c, -127.f), 127.f)), id = (int)rintf(fminf(fmaxf(d, -127.f), 127.f));
;     return (unsigned)(ia & 0xff) | ((unsigned)(ib & 0xff) << 8) | ((unsigned)(ic & 0xff) << 16) | ((unsigned)(id & 0xff) << 24);
; __device__ __forceinline__ void cvt_item_i8(const float* src, int ld, int k0, int c0, unsigned char* dst, int Kd, int drow0, const float* cmx  , unsigned char* scr, int lane) {
;     ...
; #pragma unroll
;     for (int g = 0; g < 4; ++g)
; #pragma unroll
;         for (int i = 0; i < 4; ++i) *(unsigned*)(scr + (4 * c + i) * 132 + 32 * g + 4 * q) = pack_i8x4(v[g][0][i] * inv[i], v[g][1][i] * inv[i], v[g][2][i] * inv[i], v[g][3][i] * inv[i]);
	v_mul_f32_e32 v73, v32, v73
	v_cvt_i32_f32_e32 v82, v82
	v_rndne_f32_e32 v87, v87
	v_med3_f32 v88, v88, s36, v20
	v_mul_f32_e32 v89, v32, v89
	v_cvt_i32_f32_e32 v39, v39
	v_cvt_i32_f32_sdwa v43, v43 dst_sel:WORD_1 dst_unused:UNUSED_PAD src0_sel:DWORD
	v_rndne_f32_e32 v40, v40
	v_med3_f32 v41, v41, s36, v20
	v_cvt_i32_f32_e32 v55, v55
	v_rndne_f32_e32 v56, v56
	v_med3_f32 v57, v57, s36, v20
	v_rndne_f32_e32 v29, v29
	v_med3_f32 v30, v30, s36, v20
	v_mul_f32_e32 v31, v31, v96
	v_cvt_i32_f32_sdwa v42, v42 dst_sel:BYTE_3 dst_unused:UNUSED_PAD src0_sel:DWORD
	v_rndne_f32_e32 v46, v46
	v_med3_f32 v47, v47, s36, v20
	v_mul_f32_e32 v49, v32, v49
	v_cvt_i32_f32_sdwa v58, v58 dst_sel:BYTE_3 dst_unused:UNUSED_PAD src0_sel:DWORD
	v_rndne_f32_e32 v62, v62
	v_med3_f32 v63, v63, s36, v20
	v_mul_f32_e32 v65, v32, v65
	v_cvt_i32_f32_e32 v64, v64
	v_cvt_i32_f32_sdwa v70, v70 dst_sel:WORD_1 dst_unused:UNUSED_PAD src0_sel:DWORD
	v_rndne_f32_e32 v67, v67
	v_rndne_f32_e32 v75, v75
	v_med3_f32 v68, v68, s36, v20
	v_med3_f32 v76, v76, s36, v20
	v_mul_f32_e32 v69, v32, v69
	v_mul_f32_e32 v77, v32, v77
	v_cvt_i32_f32_e32 v80, v80
	v_cvt_i32_f32_sdwa v86, v86 dst_sel:WORD_1 dst_unused:UNUSED_PAD src0_sel:DWORD
	v_rndne_f32_e32 v83, v83
	v_rndne_f32_e32 v90, v90
	v_med3_f32 v84, v84, s36, v20
	v_med3_f32 v91, v91, s36, v20
	v_mul_f32_e32 v85, v32, v85
	v_mul_f32_e32 v92, v32, v93
	v_cvt_i32_f32_e32 v35, v35
	v_rndne_f32_e32 v36, v36
	v_rndne_f32_e32 v44, v44
	v_med3_f32 v37, v37, s36, v20
	v_med3_f32 v45, v45, s36, v20
	v_cvt_i32_f32_e32 v51, v51
	v_cvt_i32_f32_sdwa v59, v59 dst_sel:WORD_1 dst_unused:UNUSED_PAD src0_sel:DWORD
	v_rndne_f32_e32 v52, v52
	v_rndne_f32_e32 v60, v60
	v_med3_f32 v53, v53, s36, v20
	v_med3_f32 v61, v61, s36, v20
	v_cvt_i32_f32_e32 v71, v71
	v_rndne_f32_e32 v72, v72
	v_med3_f32 v73, v73, s36, v20
	v_cvt_i32_f32_e32 v87, v87
	v_rndne_f32_e32 v88, v88
	v_med3_f32 v89, v89, s36, v20
	v_cvt_i32_f32_e32 v40, v40
	v_rndne_f32_e32 v41, v41
	v_cvt_i32_f32_e32 v56, v56
	v_rndne_f32_e32 v57, v57
	v_cvt_i32_f32_sdwa v74, v74 dst_sel:BYTE_3 dst_unused:UNUSED_PAD src0_sel:DWORD
	v_rndne_f32_e32 v78, v78
	v_med3_f32 v79, v79, s36, v20
	v_mul_f32_e32 v81, v32, v81
	v_cvt_i32_f32_sdwa v29, v29 dst_sel:BYTE_3 dst_unused:UNUSED_PAD src0_sel:DWORD
	v_rndne_f32_e32 v30, v30
	v_med3_f32 v31, v31, s36, v20
	v_mul_f32_e32 v32, v32, v97
	v_cvt_i32_f32_sdwa v46, v46 dst_sel:BYTE_3 dst_unused:UNUSED_PAD src0_sel:DWORD
	v_rndne_f32_e32 v47, v47
	v_med3_f32 v49, v49, s36, v20
	v_cvt_i32_f32_sdwa v62, v62 dst_sel:BYTE_3 dst_unused:UNUSED_PAD src0_sel:DWORD
	v_rndne_f32_e32 v63, v63
	v_med3_f32 v65, v65, s36, v20
	v_cvt_i32_f32_e32 v67, v67
	v_cvt_i32_f32_sdwa v75, v75 dst_sel:WORD_1 dst_unused:UNUSED_PAD src0_sel:DWORD
	v_rndne_f32_e32 v68, v68
	v_rndne_f32_e32 v76, v76
	v_med3_f32 v69, v69, s36, v20
	v_med3_f32 v77, v77, s36, v20
	v_cvt_i32_f32_e32 v83, v83
	v_cvt_i32_f32_sdwa v90, v90 dst_sel:WORD_1 dst_unused:UNUSED_PAD src0_sel:DWORD
	v_rndne_f32_e32 v84, v84
	v_rndne_f32_e32 v91, v91
	v_med3_f32 v85, v85, s36, v20
	v_med3_f32 v92, v92, s36, v20
	v_cvt_i32_f32_e32 v36, v36
	v_cvt_i32_f32_sdwa v44, v44 dst_sel:WORD_1 dst_unused:UNUSED_PAD src0_sel:DWORD
	v_rndne_f32_e32 v37, v37
	v_rndne_f32_e32 v45, v45
	v_cvt_i32_f32_e32 v52, v52
	v_cvt_i32_f32_sdwa v60, v60 dst_sel:WORD_1 dst_unused:UNUSED_PAD src0_sel:DWORD
	v_rndne_f32_e32 v53, v53
	v_rndne_f32_e32 v61, v61
	v_cvt_i32_f32_e32 v72, v72
	v_rndne_f32_e32 v73, v73
	v_cvt_i32_f32_e32 v88, v88
	v_rndne_f32_e32 v89, v89
	v_cvt_i32_f32_e32 v41, v41
	v_cvt_i32_f32_e32 v57, v57
	v_cvt_i32_f32_sdwa v78, v78 dst_sel:BYTE_3 dst_unused:UNUSED_PAD src0_sel:DWORD
	v_rndne_f32_e32 v79, v79
	v_med3_f32 v81, v81, s36, v20
	v_cvt_i32_f32_sdwa v30, v30 dst_sel:BYTE_3 dst_unused:UNUSED_PAD src0_sel:DWORD
	v_rndne_f32_e32 v31, v31
	v_med3_f32 v32, v32, s36, v20
	v_cvt_i32_f32_sdwa v47, v47 dst_sel:BYTE_3 dst_unused:UNUSED_PAD src0_sel:DWORD
	v_rndne_f32_e32 v49, v49
	v_cvt_i32_f32_sdwa v63, v63 dst_sel:BYTE_3 dst_unused:UNUSED_PAD src0_sel:DWORD
	v_rndne_f32_e32 v65, v65
	v_cvt_i32_f32_e32 v68, v68
	v_cvt_i32_f32_sdwa v76, v76 dst_sel:WORD_1 dst_unused:UNUSED_PAD src0_sel:DWORD
	v_rndne_f32_e32 v69, v69
	v_rndne_f32_e32 v77, v77
	v_cvt_i32_f32_e32 v84, v84
; __device__ __forceinline__ void cvt_item_i8(const float* src, int ld, int k0, int c0, unsigned char* dst, int Kd, int drow0, const float* cmx  , unsigned char* scr, int lane) {
;     ...
; #pragma unroll
;     for (int g = 0; g < 4; ++g)
; #pragma unroll
;         for (int i = 0; i < 4; ++i) *(unsigned*)(scr + (4 * c + i) * 132 + 32 * g + 4 * q) = pack_i8x4(v[g][0][i] * inv[i], v[g][1][i] * inv[i], v[g][2][i] * inv[i], v[g][3][i] * inv[i]);
;     asm volatile("s_waitcnt lgkmcnt(0)" ::: "memory");
; #pragma unroll
;     for (int r = 0; r < 4; ++r) { const int n = 8 * r + (lane >> 3), ch = lane & 7; const unsigned char* p = scr + n * 132 + ch * 16;
;         u32x4 o; o.x = *(const unsigned*)(p); o.y = *(const unsigned*)(p + 4); o.z = *(const unsigned*)(p + 8); o.w = *(const unsigned*)(p + 12);
;         *(u32x4*)(dst + (size_t)(drow0 + n) * Kd + k0 + 16 * ch) = o; }
;     asm volatile("s_waitcnt lgkmcnt(0)" ::: "memory");
	v_cvt_i32_f32_sdwa v91, v91 dst_sel:WORD_1 dst_unused:UNUSED_PAD src0_sel:DWORD
	v_rndne_f32_e32 v85, v85
	v_rndne_f32_e32 v92, v92
	v_cvt_i32_f32_e32 v37, v37
	v_cvt_i32_f32_sdwa v45, v45 dst_sel:WORD_1 dst_unused:UNUSED_PAD src0_sel:DWORD
	v_cvt_i32_f32_e32 v53, v53
	v_cvt_i32_f32_sdwa v61, v61 dst_sel:WORD_1 dst_unused:UNUSED_PAD src0_sel:DWORD
	v_cvt_i32_f32_e32 v73, v73
	v_cvt_i32_f32_e32 v89, v89
	v_lshlrev_b32_e32 v34, 8, v34
	v_lshlrev_b32_e32 v50, 8, v50
	v_cvt_i32_f32_sdwa v79, v79 dst_sel:BYTE_3 dst_unused:UNUSED_PAD src0_sel:DWORD
	v_rndne_f32_e32 v81, v81
	v_cvt_i32_f32_sdwa v31, v31 dst_sel:BYTE_3 dst_unused:UNUSED_PAD src0_sel:DWORD
	v_rndne_f32_e32 v32, v32
	v_cvt_i32_f32_sdwa v49, v49 dst_sel:BYTE_3 dst_unused:UNUSED_PAD src0_sel:DWORD
	v_cvt_i32_f32_sdwa v65, v65 dst_sel:BYTE_3 dst_unused:UNUSED_PAD src0_sel:DWORD
	v_cvt_i32_f32_e32 v69, v69
	v_cvt_i32_f32_sdwa v77, v77 dst_sel:WORD_1 dst_unused:UNUSED_PAD src0_sel:DWORD
	v_cvt_i32_f32_e32 v85, v85
	v_cvt_i32_f32_sdwa v92, v92 dst_sel:WORD_1 dst_unused:UNUSED_PAD src0_sel:DWORD
	v_and_b32_e32 v38, 0xff0000, v38
	v_and_b32_e32 v54, 0xff0000, v54
	v_lshlrev_b32_e32 v66, 8, v66
	v_lshlrev_b32_e32 v82, 8, v82
	v_perm_b32 v33, v34, v33, s37
	v_lshlrev_b32_e32 v34, 8, v39
	v_and_b32_e32 v39, 0xff0000, v43
	v_perm_b32 v43, v50, v48, s37
	v_lshlrev_b32_e32 v48, 8, v55
	v_cvt_i32_f32_sdwa v81, v81 dst_sel:BYTE_3 dst_unused:UNUSED_PAD src0_sel:DWORD
	v_cvt_i32_f32_sdwa v32, v32 dst_sel:BYTE_3 dst_unused:UNUSED_PAD src0_sel:DWORD
	v_and_b32_e32 v70, 0xff0000, v70
	v_and_b32_e32 v86, 0xff0000, v86
	v_and_b32_e32 v50, 0xff0000, v59
	v_perm_b32 v55, v66, v64, s37
	v_lshlrev_b32_e32 v59, 8, v71
	v_perm_b32 v66, v82, v80, s37
	v_lshlrev_b32_e32 v71, 8, v87
	v_or3_b32 v33, v33, v38, v42
	v_perm_b32 v34, v34, v35, s37
	v_lshlrev_b32_e32 v35, 8, v40
	v_or3_b32 v40, v43, v54, v58
	v_perm_b32 v42, v48, v51, s37
	v_lshlrev_b32_e32 v43, 8, v56
	v_and_b32_e32 v64, 0xff0000, v75
	v_and_b32_e32 v75, 0xff0000, v90
	v_and_b32_e32 v38, 0xff0000, v44
	v_and_b32_e32 v44, 0xff0000, v60
	v_or3_b32 v48, v55, v70, v74
	v_perm_b32 v51, v59, v67, s37
	v_lshlrev_b32_e32 v54, 8, v72
	v_or3_b32 v29, v66, v86, v29
	v_perm_b32 v56, v71, v83, s37
	v_lshlrev_b32_e32 v58, 8, v88
	v_or3_b32 v34, v34, v39, v46
	v_perm_b32 v35, v35, v36, s37
	v_lshlrev_b32_e32 v36, 8, v41
	ds_write2_b32 v21, v33, v40 offset1:8
	v_or3_b32 v33, v42, v50, v62
	v_perm_b32 v40, v43, v52, s37
	v_lshlrev_b32_e32 v41, 8, v57
	v_and_b32_e32 v55, 0xff0000, v76
	v_and_b32_e32 v59, 0xff0000, v91
	v_and_b32_e32 v39, 0xff0000, v45
	v_and_b32_e32 v42, 0xff0000, v61
	v_or3_b32 v43, v51, v64, v78
	v_perm_b32 v45, v54, v68, s37
	v_lshlrev_b32_e32 v46, 8, v73
	ds_write2_b32 v21, v48, v29 offset0:16 offset1:24
	v_or3_b32 v29, v56, v75, v30
	v_perm_b32 v30, v58, v84, s37
	v_lshlrev_b32_e32 v48, 8, v89
	v_or3_b32 v35, v35, v38, v47
	v_perm_b32 v36, v36, v37, s37
	ds_write2_b32 v21, v34, v33 offset0:33 offset1:41
	v_or3_b32 v33, v40, v44, v63
	v_perm_b32 v34, v41, v53, s37
	v_and_b32_e32 v50, 0xff0000, v77
	v_and_b32_e32 v51, 0xff0000, v92
	v_or3_b32 v37, v45, v55, v79
	v_perm_b32 v38, v46, v69, s37
	ds_write2_b32 v21, v43, v29 offset0:49 offset1:57
	v_or3_b32 v29, v30, v59, v31
	v_perm_b32 v30, v48, v85, s37
	v_or3_b32 v31, v36, v39, v49
	ds_write2_b32 v21, v35, v33 offset0:66 offset1:74
	v_or3_b32 v33, v34, v42, v65
	v_or3_b32 v34, v38, v50, v81
	ds_write2_b32 v21, v37, v29 offset0:82 offset1:90
	v_or3_b32 v29, v30, v51, v32
	ds_write2_b32 v21, v31, v33 offset0:99 offset1:107
	ds_write2_b32 v21, v34, v29 offset0:115 offset1:123
	s_waitcnt lgkmcnt(0)
	ds_read2_b32 v[30:31], v22 offset1:1
	ds_read2_b32 v[32:33], v22 offset0:2 offset1:3
	ds_read2_b32 v[34:35], v23 offset1:1
	ds_read2_b32 v[36:37], v24 offset1:1
	ds_read2_b32 v[38:39], v25 offset1:1
	ds_read2_b32 v[40:41], v26 offset1:1
	ds_read2_b32 v[42:43], v27 offset1:1
	ds_read2_b32 v[44:45], v28 offset1:1
	s_waitcnt lgkmcnt(6)
	global_store_dwordx4 v[10:11], v[30:33], off
	s_waitcnt lgkmcnt(4)
	global_store_dwordx4 v[12:13], v[34:37], off
	s_waitcnt lgkmcnt(2)
	global_store_dwordx4 v[14:15], v[38:41], off
	s_waitcnt lgkmcnt(0)
	global_store_dwordx4 v[6:7], v[42:45], off
	s_waitcnt lgkmcnt(0)
	s_cbranch_scc1 .LBB0_1909
